# attention stagger: waves 4-7 defer pack+PV of tile t to start of interval t+1 (2 barriers per tile), waves 0-3 unchanged order; SLOAD temps moved to v236-243
# speedup vs baseline: 1.0012x; 1.0001x over previous
.LBB0_707:
	v_readfirstlane_b32 s58, v0
	s_nop 3
	s_bfe_u32 s58, s58, 0x10008
	s_mov_b32 s59, 0
	s_mov_b32 s60, 0
	s_ashr_i32 s26, s19, 4
	s_sub_i32 s6, 15, s26
	s_bfe_u32 s23, s19, 0x10003
	v_readfirstlane_b32 s21, v0
	s_lshl_b32 s27, s6, 8
	s_lshl_b32 s20, s6, 2
	s_lshl_b32 s6, s23, 12
	s_lshr_b32 s21, s21, 1
	s_add_i32 s6, s27, s6
	s_and_b32 s28, s21, 0x7fffffe0
	s_add_u32 s56, s28, s6
	s_addc_u32 s57, 0, 0
	v_mov_b32_e32 v5, s57
	v_or_b32_e32 v4, s56, v216
	v_readlane_b32 s24, v254, 54
	s_lshl_b32 s6, s19, 7
	v_lshlrev_b64 v[4:5], 11, v[4:5]
	v_readlane_b32 s25, v254, 55
	s_and_b32 s21, s6, 0x380
	s_lshl_b32 s6, s21, 1
	v_lshl_add_u64 v[4:5], s[24:25], 0, v[4:5]
	s_add_i32 s22, s20, 4
	s_lshl_b32 s23, s23, 23
	v_readlane_b32 s24, v255, 0
	s_add_u32 s24, s24, s23
	v_readlane_b32 s25, v255, 1
	s_addc_u32 s25, s25, 0
	s_add_u32 s24, s24, s6
	s_addc_u32 s25, s25, 0
	v_lshl_add_u64 v[186:187], s[24:25], 0, v[184:185]
	v_readlane_b32 s24, v254, 56
	v_readlane_b32 s25, v254, 57
	s_add_u32 s23, s24, s23
	s_addc_u32 s25, s25, 0
	s_add_u32 s24, s23, s6
	s_waitcnt vmcnt(11)
	v_lshl_add_u64 v[20:21], v[4:5], 0, s[6:7]
	s_addc_u32 s25, s25, 0
	s_or_b32 s6, s20, 3
	v_lshl_add_u64 v[188:189], s[24:25], 0, v[184:185]
	s_lshl_b64 s[24:25], s[6:7], 6
	v_mov_b32_e32 v5, s25
	v_or_b32_e32 v4, s24, v193
	v_mov_b32_e32 v7, s25
	v_or_b32_e32 v6, s24, v194
	v_lshlrev_b64 v[12:13], 11, v[4:5]
	v_lshlrev_b64 v[14:15], 11, v[6:7]
	v_lshl_add_u64 v[4:5], v[186:187], 0, v[12:13]
	v_lshl_add_u64 v[8:9], v[186:187], 0, v[14:15]
	v_lshl_add_u64 v[12:13], v[188:189], 0, v[12:13]
	v_lshl_add_u64 v[16:17], v[188:189], 0, v[14:15]
	global_load_dwordx4 v[4:7], v[4:5], off
	s_nop 0
	global_load_dwordx4 v[8:11], v[8:9], off
	s_nop 0
	global_load_dwordx4 v[12:15], v[12:13], off
	s_nop 0
	global_load_dwordx4 v[16:19], v[16:17], off
	s_or_b32 s6, s20, 2
	v_lshl_add_u64 v[20:21], v[20:21], 0, v[182:183]
	s_lshl_b64 s[24:25], s[6:7], 6
	s_or_b32 s6, s20, 1
	global_load_dwordx4 v[114:117], v[20:21], off
	global_load_dwordx4 v[118:121], v[20:21], off offset:32
	global_load_dwordx4 v[122:125], v[20:21], off offset:64
	global_load_dwordx4 v[126:129], v[20:21], off offset:96
	s_waitcnt lgkmcnt(0)
	global_load_dwordx4 v[130:133], v[20:21], off offset:128
	global_load_dwordx4 v[134:137], v[20:21], off offset:160
	global_load_dwordx4 v[138:141], v[20:21], off offset:192
	global_load_dwordx4 v[142:145], v[20:21], off offset:224
	v_mov_b32_e32 v21, s25
	v_or_b32_e32 v20, s24, v193
	s_waitcnt vmcnt(22)
	v_mov_b32_e32 v23, s25
	v_or_b32_e32 v22, s24, v194
	s_lshl_b64 s[24:25], s[6:7], 6
	v_lshlrev_b64 v[20:21], 11, v[20:21]
	v_mov_b32_e32 v25, s25
	v_or_b32_e32 v24, s24, v193
	s_waitcnt vmcnt(21)
	v_mov_b32_e32 v27, s25
	v_or_b32_e32 v26, s24, v194
	v_lshlrev_b64 v[22:23], 11, v[22:23]
	v_lshl_add_u64 v[28:29], v[186:187], 0, v[20:21]
	v_lshlrev_b64 v[24:25], 11, v[24:25]
	v_lshlrev_b64 v[26:27], 11, v[26:27]
	s_waitcnt vmcnt(20)
	v_lshl_add_u64 v[30:31], v[186:187], 0, v[22:23]
	v_lshl_add_u64 v[20:21], v[188:189], 0, v[20:21]
	v_lshl_add_u64 v[22:23], v[188:189], 0, v[22:23]
	v_lshl_add_u64 v[32:33], v[186:187], 0, v[24:25]
	s_waitcnt vmcnt(19)
	v_lshl_add_u64 v[34:35], v[186:187], 0, v[26:27]
	v_lshl_add_u64 v[24:25], v[188:189], 0, v[24:25]
	v_lshl_add_u64 v[26:27], v[188:189], 0, v[26:27]
	s_add_i32 s23, s28, s27
	s_lshl_b32 s6, s26, 8
	v_mov_b32_e32 v3, v2
	v_or_b32_e32 v234, s23, v216
	s_or_b32 s24, s23, 31
	s_sub_i32 s25, 0xf80, s6
	v_mov_b32_e32 v191, 1.0
	s_mov_b32 s6, s20
	s_mov_b32 s26, s7
	s_waitcnt vmcnt(11)
	ds_write_b128 v229, v[4:7]
	s_waitcnt vmcnt(10)
	ds_write_b128 v230, v[8:11]
	s_waitcnt vmcnt(9)
	ds_write_b128 v231, v[12:15] offset:32768
	s_waitcnt vmcnt(8)
	ds_write_b128 v232, v[16:19] offset:32768
	s_waitcnt lgkmcnt(0)
	s_barrier
	global_load_dwordx4 v[146:149], v[28:29], off
	global_load_dwordx4 v[150:153], v[30:31], off
	global_load_dwordx4 v[158:161], v[20:21], off
	global_load_dwordx4 v[166:169], v[22:23], off
	global_load_dwordx4 v[154:157], v[32:33], off
	global_load_dwordx4 v[162:165], v[34:35], off
	global_load_dwordx4 v[170:173], v[24:25], off
	global_load_dwordx4 v[174:177], v[26:27], off
	v_mov_b32_e32 v16, v2
	v_mov_b32_e32 v17, v2
	v_mov_b32_e32 v4, v2
	v_mov_b32_e32 v5, v2
	v_mov_b32_e32 v6, v2
	v_mov_b32_e32 v7, v2
	v_mov_b32_e32 v8, v2
	v_mov_b32_e32 v9, v2
	v_mov_b32_e32 v10, v2
	v_mov_b32_e32 v11, v2
	v_mov_b32_e32 v12, v2
	v_mov_b32_e32 v13, v2
	v_mov_b32_e32 v14, v2
	v_mov_b32_e32 v15, v2
	v_mov_b64_e32 v[32:33], v[16:17]
	v_mov_b64_e32 v[48:49], v[16:17]
	v_mov_b64_e32 v[64:65], v[16:17]
	v_mov_b64_e32 v[80:81], v[16:17]
	v_mov_b64_e32 v[30:31], v[14:15]
	v_mov_b64_e32 v[28:29], v[12:13]
	v_mov_b64_e32 v[26:27], v[10:11]
	v_mov_b64_e32 v[24:25], v[8:9]
	v_mov_b64_e32 v[22:23], v[6:7]
	v_mov_b64_e32 v[20:21], v[4:5]
	v_mov_b64_e32 v[18:19], v[2:3]
	v_mov_b64_e32 v[46:47], v[14:15]
	v_mov_b64_e32 v[44:45], v[12:13]
	v_mov_b64_e32 v[42:43], v[10:11]
	v_mov_b64_e32 v[40:41], v[8:9]
	v_mov_b64_e32 v[38:39], v[6:7]
	v_mov_b64_e32 v[36:37], v[4:5]
	v_mov_b64_e32 v[34:35], v[2:3]
	v_mov_b64_e32 v[62:63], v[14:15]
	v_mov_b64_e32 v[60:61], v[12:13]
	v_mov_b64_e32 v[58:59], v[10:11]
	v_mov_b64_e32 v[56:57], v[8:9]
	v_mov_b64_e32 v[54:55], v[6:7]
	v_mov_b64_e32 v[52:53], v[4:5]
	v_mov_b64_e32 v[50:51], v[2:3]
	v_mov_b64_e32 v[78:79], v[14:15]
	v_mov_b64_e32 v[76:77], v[12:13]
	v_mov_b64_e32 v[74:75], v[10:11]
	v_mov_b64_e32 v[72:73], v[8:9]
	v_mov_b64_e32 v[70:71], v[6:7]
	v_mov_b64_e32 v[68:69], v[4:5]
	v_mov_b64_e32 v[66:67], v[2:3]
	s_add_i32 s27, s25, 64
	s_cmp_ge_i32 s27, s24
	s_cbranch_scc1 .Lst0_skip0
	s_branch .Lst0_b0
.Lst0_skip0:
	s_barrier
	s_branch .LBB0_712
.Lst0_pre0:
	s_cmp_eq_u32 s59, 2
	s_cbranch_scc0 .Lst0_ret0
	s_mov_b32 s59, 0
	s_mov_b32 s60, 1
	s_branch .Lst0_tail1

.Lst0_pre1:
	s_cmp_eq_u32 s59, 1
	s_cbranch_scc0 .Lst0_ret1
	s_mov_b32 s59, 0
	s_mov_b32 s60, 1
	s_branch .Lst0_tail0

.Lst0_b0:
	s_cmp_lg_u32 s58, 0
	s_cbranch_scc1 .Lst0_pre0
.LBB0_709:
	v_add_u32_e32 v3, v219, v220
	ds_read_b128 v[4:7], v3
	ds_read_b128 v[8:11], v3 offset:8192
	v_add_u32_e32 v3, v219, v221
	ds_read_b128 v[236:239], v3
	ds_read_b128 v[240:243], v3 offset:8192
	v_add_u32_e32 v3, v219, v222
	ds_read_b128 v[244:247], v3
	ds_read_b128 v[248:251], v3 offset:8192
	s_add_i32 s27, s25, 0x7f
	s_cmp_lt_i32 s27, s23
	v_add_u32_e32 v3, v219, v223
	s_waitcnt vmcnt(15) lgkmcnt(5)
	v_mfma_f32_32x32x16_bf16 v[82:97], v[4:7], v[114:117], 0
	s_waitcnt lgkmcnt(4)
	v_mfma_f32_32x32x16_bf16 v[98:113], v[8:11], v[114:117], 0
	ds_read_b128 v[4:7], v3
	ds_read_b128 v[8:11], v3 offset:8192
	v_add_u32_e32 v3, v219, v224
	s_waitcnt vmcnt(14) lgkmcnt(5)
	v_mfma_f32_32x32x16_bf16 v[82:97], v[236:239], v[118:121], v[82:97]
	s_waitcnt lgkmcnt(4)
	v_mfma_f32_32x32x16_bf16 v[98:113], v[240:243], v[118:121], v[98:113]
	ds_read_b128 v[236:239], v3
	ds_read_b128 v[240:243], v3 offset:8192
	v_add_u32_e32 v3, v219, v225
	s_waitcnt vmcnt(13) lgkmcnt(5)
	v_mfma_f32_32x32x16_bf16 v[82:97], v[244:247], v[122:125], v[82:97]
	s_waitcnt lgkmcnt(4)
	v_mfma_f32_32x32x16_bf16 v[98:113], v[248:251], v[122:125], v[98:113]
	ds_read_b128 v[244:247], v3
	ds_read_b128 v[248:251], v3 offset:8192
	v_add_u32_e32 v3, v219, v226
	s_waitcnt vmcnt(12) lgkmcnt(5)
	v_mfma_f32_32x32x16_bf16 v[82:97], v[4:7], v[126:129], v[82:97]
	s_waitcnt lgkmcnt(4)
	v_mfma_f32_32x32x16_bf16 v[98:113], v[8:11], v[126:129], v[98:113]
	ds_read_b128 v[4:7], v3
	ds_read_b128 v[8:11], v3 offset:8192
	v_add_u32_e32 v3, v219, v227
	s_waitcnt vmcnt(11) lgkmcnt(5)
	v_mfma_f32_32x32x16_bf16 v[82:97], v[236:239], v[130:133], v[82:97]
	s_waitcnt lgkmcnt(4)
	v_mfma_f32_32x32x16_bf16 v[98:113], v[240:243], v[130:133], v[98:113]
	ds_read_b128 v[236:239], v3
	ds_read_b128 v[240:243], v3 offset:8192
	s_waitcnt vmcnt(10) lgkmcnt(5)
	v_mfma_f32_32x32x16_bf16 v[82:97], v[244:247], v[134:137], v[82:97]
	s_waitcnt lgkmcnt(4)
	v_mfma_f32_32x32x16_bf16 v[98:113], v[248:251], v[134:137], v[98:113]
	s_waitcnt vmcnt(9) lgkmcnt(3)
	v_mfma_f32_32x32x16_bf16 v[82:97], v[4:7], v[138:141], v[82:97]
	s_waitcnt lgkmcnt(2)
	v_mfma_f32_32x32x16_bf16 v[98:113], v[8:11], v[138:141], v[98:113]
	s_waitcnt vmcnt(8) lgkmcnt(1)
	v_mfma_f32_32x32x16_bf16 v[82:97], v[236:239], v[142:145], v[82:97]
	s_waitcnt lgkmcnt(0)
	v_mfma_f32_32x32x16_bf16 v[98:113], v[240:243], v[142:145], v[98:113]
	s_cmp_lg_u32 s58, 0
	s_cbranch_scc1 .Lst0_nob2_0
	s_barrier
.Lst0_nob2_0:
	s_add_i32 s27, s25, 0x7f
	s_cmp_lt_i32 s27, s23
	s_cbranch_scc1 .LBB0_711
	v_add_u32_e32 v3, s25, v217
	v_add_u32_e32 v4, 64, v3
	v_cmp_lt_i32_e32 vcc, v4, v234
	v_add_u32_e32 v4, 0x60, v3
	s_nop 4
	v_cndmask_b32_e32 v82, v233, v82, vcc
	v_cmp_lt_i32_e32 vcc, v4, v234
	v_add_u32_e32 v4, 0x41, v3
	s_nop 0
	v_cndmask_b32_e32 v98, v233, v98, vcc
	v_cmp_lt_i32_e32 vcc, v4, v234
	v_add_u32_e32 v4, 0x61, v3
	s_nop 0
	v_cndmask_b32_e32 v83, v233, v83, vcc
	v_cmp_lt_i32_e32 vcc, v4, v234
	v_add_u32_e32 v4, 0x42, v3
	s_nop 0
	v_cndmask_b32_e32 v99, v233, v99, vcc
	v_cmp_lt_i32_e32 vcc, v4, v234
	v_add_u32_e32 v4, 0x62, v3
	s_nop 0
	v_cndmask_b32_e32 v84, v233, v84, vcc
	v_cmp_lt_i32_e32 vcc, v4, v234
	v_add_u32_e32 v4, 0x43, v3
	s_nop 0
	v_cndmask_b32_e32 v100, v233, v100, vcc
	v_cmp_lt_i32_e32 vcc, v4, v234
	v_add_u32_e32 v4, 0x63, v3
	s_nop 0
	v_cndmask_b32_e32 v85, v233, v85, vcc
	v_cmp_lt_i32_e32 vcc, v4, v234
	v_add_u32_e32 v4, 0x48, v3
	s_nop 0
	v_cndmask_b32_e32 v101, v233, v101, vcc
	v_cmp_lt_i32_e32 vcc, v4, v234
	v_add_u32_e32 v4, 0x68, v3
	s_nop 0
	v_cndmask_b32_e32 v86, v233, v86, vcc
	v_cmp_lt_i32_e32 vcc, v4, v234
	v_add_u32_e32 v4, 0x49, v3
	s_nop 0
	v_cndmask_b32_e32 v102, v233, v102, vcc
	v_cmp_lt_i32_e32 vcc, v4, v234
	v_add_u32_e32 v4, 0x69, v3
	s_nop 0
	v_cndmask_b32_e32 v87, v233, v87, vcc
	v_cmp_lt_i32_e32 vcc, v4, v234
	v_add_u32_e32 v4, 0x4a, v3
	s_nop 0
	v_cndmask_b32_e32 v103, v233, v103, vcc
	v_cmp_lt_i32_e32 vcc, v4, v234
	v_add_u32_e32 v4, 0x6a, v3
	s_nop 0
	v_cndmask_b32_e32 v88, v233, v88, vcc
	v_cmp_lt_i32_e32 vcc, v4, v234
	v_add_u32_e32 v4, 0x4b, v3
	s_nop 0
	v_cndmask_b32_e32 v104, v233, v104, vcc
	v_cmp_lt_i32_e32 vcc, v4, v234
	v_add_u32_e32 v4, 0x6b, v3
	s_nop 0
	v_cndmask_b32_e32 v89, v233, v89, vcc
	v_cmp_lt_i32_e32 vcc, v4, v234
	v_add_u32_e32 v4, 0x50, v3
	s_nop 0
	v_cndmask_b32_e32 v105, v233, v105, vcc
	v_cmp_lt_i32_e32 vcc, v4, v234
	v_add_u32_e32 v4, 0x70, v3
	s_nop 0
	v_cndmask_b32_e32 v90, v233, v90, vcc
	v_cmp_lt_i32_e32 vcc, v4, v234
	v_add_u32_e32 v4, 0x51, v3
	s_nop 0
	v_cndmask_b32_e32 v106, v233, v106, vcc
	v_cmp_lt_i32_e32 vcc, v4, v234
	v_add_u32_e32 v4, 0x71, v3
	s_nop 0
	v_cndmask_b32_e32 v91, v233, v91, vcc
	v_cmp_lt_i32_e32 vcc, v4, v234
	v_add_u32_e32 v4, 0x52, v3
	s_nop 0
	v_cndmask_b32_e32 v107, v233, v107, vcc
	v_cmp_lt_i32_e32 vcc, v4, v234
	v_add_u32_e32 v4, 0x72, v3
	s_nop 0
	v_cndmask_b32_e32 v92, v233, v92, vcc
	v_cmp_lt_i32_e32 vcc, v4, v234
	v_add_u32_e32 v4, 0x53, v3
	s_nop 0
	v_cndmask_b32_e32 v108, v233, v108, vcc
	v_cmp_lt_i32_e32 vcc, v4, v234
	v_add_u32_e32 v4, 0x73, v3
	s_nop 0
	v_cndmask_b32_e32 v93, v233, v93, vcc
	v_cmp_lt_i32_e32 vcc, v4, v234
	v_add_u32_e32 v4, 0x58, v3
	s_nop 0
	v_cndmask_b32_e32 v109, v233, v109, vcc
	v_cmp_lt_i32_e32 vcc, v4, v234
	v_add_u32_e32 v4, 0x78, v3
	s_nop 0
	v_cndmask_b32_e32 v94, v233, v94, vcc
	v_cmp_lt_i32_e32 vcc, v4, v234
	v_add_u32_e32 v4, 0x59, v3
	s_nop 0
	v_cndmask_b32_e32 v110, v233, v110, vcc
	v_cmp_lt_i32_e32 vcc, v4, v234
	v_add_u32_e32 v4, 0x79, v3
	s_nop 0
	v_cndmask_b32_e32 v95, v233, v95, vcc
	v_cmp_lt_i32_e32 vcc, v4, v234
	v_add_u32_e32 v4, 0x5a, v3
	s_nop 0
	v_cndmask_b32_e32 v111, v233, v111, vcc
	v_cmp_lt_i32_e32 vcc, v4, v234
	v_add_u32_e32 v4, 0x7a, v3
	s_nop 0
	v_cndmask_b32_e32 v96, v233, v96, vcc
	v_cmp_lt_i32_e32 vcc, v4, v234
	v_add_u32_e32 v4, 0x5b, v3
	v_add_u32_e32 v3, 0x7b, v3
	v_cndmask_b32_e32 v112, v233, v112, vcc
	v_cmp_lt_i32_e32 vcc, v4, v234
	s_nop 1
	v_cndmask_b32_e32 v97, v233, v97, vcc
	v_cmp_lt_i32_e32 vcc, v3, v234
	s_nop 1
	v_cndmask_b32_e32 v113, v233, v113, vcc
.LBB0_711:
	s_nop 10
	v_exp_f32_e32 v3, v98
	v_exp_f32_e32 v4, v82
	v_exp_f32_e32 v98, v112
	v_exp_f32_e32 v6, v99
	v_add_f32_e32 v3, 1.0, v3
	v_add_f32_e32 v5, 1.0, v4
	v_rcp_f32_e32 v4, v3
	v_exp_f32_e32 v3, v83
	v_exp_f32_e32 v99, v97
	v_exp_f32_e32 v16, v104
	v_exp_f32_e32 v82, v105
	v_add_f32_e32 v3, 1.0, v3
	v_rcp_f32_e32 v7, v3
	v_exp_f32_e32 v3, v84
	v_exp_f32_e32 v84, v106
	v_exp_f32_e32 v8, v100
	v_exp_f32_e32 v10, v101
	v_add_f32_e32 v3, 1.0, v3
	v_rcp_f32_e32 v9, v3
	v_exp_f32_e32 v3, v85
	v_exp_f32_e32 v14, v103
	v_exp_f32_e32 v12, v102
	v_add_f32_e32 v84, 1.0, v84
	v_add_f32_e32 v3, 1.0, v3
	v_rcp_f32_e32 v11, v3
	v_exp_f32_e32 v3, v86
	v_exp_f32_e32 v86, v107
	v_rcp_f32_e32 v84, v84
	v_add_f32_e32 v16, 1.0, v16
	v_add_f32_e32 v3, 1.0, v3
	v_rcp_f32_e32 v13, v3
	v_exp_f32_e32 v3, v87
	v_add_f32_e32 v86, 1.0, v86
	v_rcp_f32_e32 v86, v86
	v_add_f32_e32 v82, 1.0, v82
	v_add_f32_e32 v3, 1.0, v3
	v_rcp_f32_e32 v15, v3
	v_exp_f32_e32 v3, v88
	v_exp_f32_e32 v88, v108
	v_add_f32_e32 v8, 1.0, v8
	v_add_f32_e32 v10, 1.0, v10
	v_add_f32_e32 v3, 1.0, v3
	v_rcp_f32_e32 v17, v3
	v_exp_f32_e32 v3, v89
	v_add_f32_e32 v88, 1.0, v88
	v_rcp_f32_e32 v88, v88
	v_add_f32_e32 v14, 1.0, v14
	v_add_f32_e32 v3, 1.0, v3
	v_rcp_f32_e32 v83, v3
	v_exp_f32_e32 v3, v90
	v_exp_f32_e32 v90, v109
	v_rcp_f32_e32 v16, v16
	v_rcp_f32_e32 v82, v82
	v_add_f32_e32 v3, 1.0, v3
	v_rcp_f32_e32 v85, v3
	v_exp_f32_e32 v3, v91
	v_add_f32_e32 v90, 1.0, v90
	v_rcp_f32_e32 v90, v90
	v_add_f32_e32 v6, 1.0, v6
	v_add_f32_e32 v3, 1.0, v3
	v_rcp_f32_e32 v87, v3
	v_exp_f32_e32 v3, v92
	v_exp_f32_e32 v92, v110
	v_rcp_f32_e32 v8, v8
	v_rcp_f32_e32 v10, v10
	v_add_f32_e32 v3, 1.0, v3
	v_rcp_f32_e32 v89, v3
	v_exp_f32_e32 v3, v93
	v_add_f32_e32 v92, 1.0, v92
	v_rcp_f32_e32 v92, v92
	v_add_f32_e32 v12, 1.0, v12
	v_add_f32_e32 v3, 1.0, v3
	v_rcp_f32_e32 v91, v3
	v_exp_f32_e32 v3, v94
	v_exp_f32_e32 v94, v111
	v_rcp_f32_e32 v14, v14
	v_pk_mul_f32 v[238:239], v[88:89], v[90:91]
	v_add_f32_e32 v3, 1.0, v3
	v_rcp_f32_e32 v93, v3
	v_exp_f32_e32 v3, v95
	v_add_f32_e32 v94, 1.0, v94
	v_rcp_f32_e32 v94, v94
	v_pk_mul_f32 v[240:241], v[86:87], v[238:239]
	v_add_f32_e32 v3, 1.0, v3
	v_rcp_f32_e32 v95, v3
	v_exp_f32_e32 v3, v96
	v_add_f32_e32 v96, 1.0, v98
	v_exp_f32_e32 v98, v113
	v_rcp_f32_e32 v96, v96
	v_add_f32_e32 v3, 1.0, v3
	v_rcp_f32_e32 v97, v3
	v_add_f32_e32 v3, 1.0, v98
	v_rcp_f32_e32 v98, v3
	v_add_f32_e32 v3, 1.0, v99
	v_rcp_f32_e32 v99, v3
	v_rcp_f32_e32 v6, v6
	v_rcp_f32_e32 v12, v12
	v_pk_mul_f32 v[242:243], v[84:85], v[240:241]
	v_pk_mul_f32 v[248:249], v[96:97], v[98:99]
	v_rcp_f32_e32 v5, v5
	v_pk_mul_f32 v[250:251], v[94:95], v[248:249]
	v_mov_b32_e32 v244, v242
	v_pk_mul_f32 v[252:253], v[92:93], v[250:251]
	v_pk_mul_f32 v[110:111], v[16:17], v[82:83]
	v_mov_b32_e32 v104, v252
	v_permlane32_swap_b32_e32 v242, v244
	s_nop 0
	v_permlane32_swap_b32_e32 v252, v104
	v_pk_mul_f32 v[100:101], v[8:9], v[10:11]
	v_pk_mul_f32 v[112:113], v[14:15], v[110:111]
	v_mul_f32_e32 v105, v191, v104
	v_mul_f32_e32 v245, v252, v104
	v_mov_b32_e32 v190, v242
	v_pk_mul_f32 v[102:103], v[6:7], v[100:101]
	v_pk_mul_f32 v[236:237], v[12:13], v[112:113]
	v_cndmask_b32_e64 v214, v191, v105, s[2:3]
	v_pk_mul_f32 v[190:191], v[190:191], v[244:245]
	v_pk_mul_f32 v[106:107], v[4:5], v[102:103]
	v_mov_b32_e32 v3, v236
	v_mul_f32_e32 v104, v191, v244
	v_mov_b32_e32 v206, v106
	v_permlane32_swap_b32_e32 v236, v3
	v_cndmask_b32_e64 v242, v191, v104, s[2:3]
	v_pk_mul_f32 v[190:191], v[190:191], v[190:191] op_sel:[0,1] op_sel_hi:[1,0]
	v_permlane32_swap_b32_e32 v106, v206
	v_mul_f32_e32 v104, v190, v3
	v_cndmask_b32_e64 v244, v190, v104, s[2:3]
	v_mul_f32_e32 v105, v236, v3
	v_mov_b32_e32 v104, v106
	v_mov_b32_e32 v207, v190
	v_pk_mul_f32 v[104:105], v[104:105], v[206:207]
	v_mov_b32_e32 v246, v243
	v_mov_b32_e32 v247, v253
	v_mul_f32_e32 v3, v105, v206
	v_permlane32_swap_b32_e32 v243, v246
	v_permlane32_swap_b32_e32 v253, v247
	v_cndmask_b32_e64 v106, v105, v3, s[2:3]
	v_pk_mul_f32 v[104:105], v[104:105], v[104:105] op_sel:[0,1] op_sel_hi:[1,0]
	v_mul_f32_e32 v191, v253, v247
	v_mul_f32_e32 v3, v104, v247
	v_mov_b32_e32 v190, v243
	v_mov_b32_e32 v247, v104
	v_cndmask_b32_e64 v215, v104, v3, s[2:3]
	v_pk_mul_f32 v[104:105], v[190:191], v[246:247]
	v_mov_b32_e32 v108, v107
	v_mov_b32_e32 v109, v237
	v_mul_f32_e32 v3, v105, v246
	v_permlane32_swap_b32_e32 v107, v108
	v_permlane32_swap_b32_e32 v237, v109
	v_cndmask_b32_e64 v243, v105, v3, s[2:3]
	v_pk_mul_f32 v[104:105], v[104:105], v[104:105] op_sel:[0,1] op_sel_hi:[1,0]
	v_mul_f32_e32 v191, v237, v109
	v_mul_f32_e32 v3, v104, v109
	v_mov_b32_e32 v190, v107
	v_mov_b32_e32 v109, v104
	v_cndmask_b32_e64 v245, v104, v3, s[2:3]
	v_pk_mul_f32 v[104:105], v[190:191], v[108:109]
	s_nop 0
	v_mul_f32_e32 v3, v105, v108
	v_cndmask_b32_e64 v107, v105, v3, s[2:3]
	v_mul_f32_e32 v191, v104, v105
	v_pk_mul_f32 v[104:105], v[10:11], v[106:107]
	v_pk_mul_f32 v[100:101], v[100:101], v[106:107]
	v_pk_mul_f32 v[102:103], v[102:103], v[106:107]
	v_pk_fma_f32 v[104:105], v[8:9], v[104:105], v[104:105] neg_lo:[1,0,0] neg_hi:[1,0,0]
	v_pk_fma_f32 v[100:101], v[6:7], v[100:101], v[100:101] neg_lo:[1,0,0] neg_hi:[1,0,0]
	v_pk_mul_f32 v[6:7], v[110:111], v[244:245]
	v_pk_mul_f32 v[8:9], v[112:113], v[244:245]
	v_pk_fma_f32 v[102:103], v[4:5], v[102:103], v[102:103] neg_lo:[1,0,0] neg_hi:[1,0,0]
	v_pk_mul_f32 v[4:5], v[82:83], v[244:245]
	v_pk_fma_f32 v[14:15], v[14:15], v[6:7], v[6:7] neg_lo:[1,0,0] neg_hi:[1,0,0]
	v_pk_fma_f32 v[108:109], v[12:13], v[8:9], v[8:9] neg_lo:[1,0,0] neg_hi:[1,0,0]
	v_pk_mul_f32 v[6:7], v[238:239], v[242:243]
	v_pk_mul_f32 v[8:9], v[240:241], v[242:243]
	v_pk_fma_f32 v[82:83], v[82:83], v[244:245], v[244:245] neg_lo:[1,0,0] neg_hi:[1,0,0]
	v_pk_fma_f32 v[16:17], v[16:17], v[4:5], v[4:5] neg_lo:[1,0,0] neg_hi:[1,0,0]
	v_pk_mul_f32 v[4:5], v[90:91], v[242:243]
	v_pk_fma_f32 v[86:87], v[86:87], v[6:7], v[6:7] neg_lo:[1,0,0] neg_hi:[1,0,0]
	v_pk_fma_f32 v[84:85], v[84:85], v[8:9], v[8:9] neg_lo:[1,0,0] neg_hi:[1,0,0]
	v_pk_mul_f32 v[6:7], v[248:249], v[214:215]
	v_pk_mul_f32 v[8:9], v[250:251], v[214:215]
	v_pk_fma_f32 v[90:91], v[90:91], v[242:243], v[242:243] neg_lo:[1,0,0] neg_hi:[1,0,0]
	v_pk_fma_f32 v[88:89], v[88:89], v[4:5], v[4:5] neg_lo:[1,0,0] neg_hi:[1,0,0]
	v_pk_fma_f32 v[94:95], v[94:95], v[6:7], v[6:7] neg_lo:[1,0,0] neg_hi:[1,0,0]
	v_pk_fma_f32 v[92:93], v[92:93], v[8:9], v[8:9] neg_lo:[1,0,0] neg_hi:[1,0,0]
	s_cmp_lg_u32 s58, 0
	s_cbranch_scc0 .Lst0_tail0
	s_mov_b32 s59, 1
	s_branch .LBB0_712
.Lst0_tail0:
	v_cvt_pk_bf16_f32 v6, v109, v15
	v_cvt_pk_bf16_f32 v8, v85, v87
	v_cvt_pk_bf16_f32 v15, v16, v82
	v_cvt_pk_bf16_f32 v82, v84, v86
	ds_read_b64_tr_b16 v[86:87], v218 offset:0
	v_cvt_pk_bf16_f32 v7, v17, v83
	v_cvt_pk_bf16_f32 v9, v89, v91
	v_cvt_pk_bf16_f32 v83, v88, v90
	ds_read_b64_tr_b16 v[88:89], v218 offset:0x800
	ds_read_b64_tr_b16 v[90:91], v218 offset:0x1000
	v_pk_fma_f32 v[106:107], v[10:11], v[106:107], v[106:107] neg_lo:[1,0,0] neg_hi:[1,0,0]
	v_pk_mul_f32 v[4:5], v[98:99], v[214:215]
	v_cvt_pk_bf16_f32 v10, v93, v95
	v_cvt_pk_bf16_f32 v84, v92, v94
	ds_read_b64_tr_b16 v[92:93], v218 offset:0x1800
	v_pk_fma_f32 v[98:99], v[98:99], v[214:215], v[214:215] neg_lo:[1,0,0] neg_hi:[1,0,0]
	v_pk_fma_f32 v[96:97], v[96:97], v[4:5], v[4:5] neg_lo:[1,0,0] neg_hi:[1,0,0]
	ds_read_b64_tr_b16 v[94:95], v218 offset:0x2000
	v_cvt_pk_bf16_f32 v4, v103, v101
	v_cvt_pk_bf16_f32 v11, v97, v99
	v_cvt_pk_bf16_f32 v85, v96, v98
	ds_read_b64_tr_b16 v[96:97], v218 offset:0x2800
	ds_read_b64_tr_b16 v[98:99], v218 offset:0x3000
	v_cvt_pk_bf16_f32 v12, v102, v100
	ds_read_b64_tr_b16 v[100:101], v218 offset:0x3800
	s_waitcnt lgkmcnt(0)
	v_cvt_pk_bf16_f32 v5, v105, v107
	v_cvt_pk_bf16_f32 v13, v104, v106
	v_cvt_pk_bf16_f32 v14, v108, v14
	v_permlane32_swap_b32_e32 v4, v6
	v_permlane32_swap_b32_e32 v5, v7
	v_permlane32_swap_b32_e32 v8, v10
	v_permlane32_swap_b32_e32 v9, v11
	v_permlane32_swap_b32_e32 v12, v14
	v_permlane32_swap_b32_e32 v13, v15
	v_permlane32_swap_b32_e32 v82, v84
	v_permlane32_swap_b32_e32 v83, v85
	v_mfma_f32_32x32x16_bf16 v[66:81], v[4:7], v[86:89], v[66:81]
	ds_read_b64_tr_b16 v[86:87], v218 offset:0x200
	ds_read_b64_tr_b16 v[88:89], v218 offset:0xa00
	v_mfma_f32_32x32x16_bf16 v[66:81], v[8:11], v[90:93], v[66:81]
	ds_read_b64_tr_b16 v[90:91], v218 offset:0x1200
	ds_read_b64_tr_b16 v[92:93], v218 offset:0x1a00
	v_mfma_f32_32x32x16_bf16 v[66:81], v[12:15], v[94:97], v[66:81]
	ds_read_b64_tr_b16 v[94:95], v218 offset:0x2200
	ds_read_b64_tr_b16 v[96:97], v218 offset:0x2a00
	ds_read_b64_tr_b16 v[102:103], v218 offset:0x3200
	ds_read_b64_tr_b16 v[104:105], v218 offset:0x3a00
	s_waitcnt lgkmcnt(0)
	v_mfma_f32_32x32x16_bf16 v[66:81], v[82:85], v[98:101], v[66:81]
	v_mfma_f32_32x32x16_bf16 v[50:65], v[4:7], v[86:89], v[50:65]
	ds_read_b64_tr_b16 v[86:87], v218 offset:0x400
	ds_read_b64_tr_b16 v[88:89], v218 offset:0xc00
	v_mfma_f32_32x32x16_bf16 v[50:65], v[8:11], v[90:93], v[50:65]
	ds_read_b64_tr_b16 v[90:91], v218 offset:0x1400
	ds_read_b64_tr_b16 v[92:93], v218 offset:0x1c00
	v_mfma_f32_32x32x16_bf16 v[50:65], v[12:15], v[94:97], v[50:65]
	ds_read_b64_tr_b16 v[94:95], v218 offset:0x2400
	ds_read_b64_tr_b16 v[96:97], v218 offset:0x2c00
	ds_read_b64_tr_b16 v[98:99], v218 offset:0x3400
	ds_read_b64_tr_b16 v[100:101], v218 offset:0x3c00
	s_waitcnt lgkmcnt(0)
	v_mfma_f32_32x32x16_bf16 v[50:65], v[82:85], v[102:105], v[50:65]
	v_mfma_f32_32x32x16_bf16 v[34:49], v[4:7], v[86:89], v[34:49]
	ds_read_b64_tr_b16 v[86:87], v218 offset:0x600
	ds_read_b64_tr_b16 v[88:89], v218 offset:0xe00
	v_mfma_f32_32x32x16_bf16 v[34:49], v[8:11], v[90:93], v[34:49]
	ds_read_b64_tr_b16 v[90:91], v218 offset:0x1600
	ds_read_b64_tr_b16 v[92:93], v218 offset:0x1e00
	v_mfma_f32_32x32x16_bf16 v[34:49], v[12:15], v[94:97], v[34:49]
	ds_read_b64_tr_b16 v[94:95], v218 offset:0x2600
	ds_read_b64_tr_b16 v[96:97], v218 offset:0x2e00
	ds_read_b64_tr_b16 v[102:103], v218 offset:0x3600
	ds_read_b64_tr_b16 v[104:105], v218 offset:0x3e00
	s_waitcnt lgkmcnt(0)
	v_mfma_f32_32x32x16_bf16 v[34:49], v[82:85], v[98:101], v[34:49]
	v_mfma_f32_32x32x16_bf16 v[18:33], v[4:7], v[86:89], v[18:33]
	v_mfma_f32_32x32x16_bf16 v[18:33], v[8:11], v[90:93], v[18:33]
	v_mfma_f32_32x32x16_bf16 v[18:33], v[12:15], v[94:97], v[18:33]
	v_mfma_f32_32x32x16_bf16 v[18:33], v[82:85], v[102:105], v[18:33]
	s_cmp_lg_u32 s60, 0
	s_cbranch_scc0 .LBB0_712
	s_cmp_eq_u32 s60, 2
	s_mov_b32 s60, 0
	s_cbranch_scc1 .Lst0_epi
	s_branch .Lst0_ret1
.LBB0_712:
	s_waitcnt vmcnt(3)
	ds_write_b128 v229, v[146:149] offset:16384
	s_waitcnt vmcnt(2)
	ds_write_b128 v230, v[150:153] offset:16384
	s_waitcnt vmcnt(1)
	ds_write_b128 v231, v[158:161] offset:49152
	s_waitcnt vmcnt(0)
	ds_write_b128 v232, v[166:169] offset:49152
	s_waitcnt lgkmcnt(0)
	s_cmp_gt_u32 s26, s20
	s_barrier
	s_cbranch_scc1 .LBB0_714
	s_lshl_b64 s[28:29], s[6:7], 6
	v_mov_b32_e32 v237, s29
	v_or_b32_e32 v236, s28, v193
	v_lshlrev_b64 v[236:237], 11, v[236:237]
	v_mov_b32_e32 v241, s29
	v_or_b32_e32 v240, s28, v194
	v_lshl_add_u64 v[238:239], v[186:187], 0, v[236:237]
	v_lshlrev_b64 v[240:241], 11, v[240:241]
	v_lshl_add_u64 v[236:237], v[188:189], 0, v[236:237]
	v_lshl_add_u64 v[242:243], v[186:187], 0, v[240:241]
	global_load_dwordx4 v[146:149], v[238:239], off
	global_load_dwordx4 v[150:153], v[242:243], off
	v_lshl_add_u64 v[238:239], v[188:189], 0, v[240:241]
	global_load_dwordx4 v[158:161], v[236:237], off
	global_load_dwordx4 v[166:169], v[238:239], off
.LBB0_714:
	s_cmp_ge_i32 s25, s24
	s_cbranch_scc1 .Lst0_skip1
	s_cmp_lg_u32 s58, 0
	s_cbranch_scc1 .Lst0_pre1
.Lst0_qk1:
	v_add_u32_e32 v3, v219, v220
	ds_read_b128 v[4:7], v3 offset:16384
	ds_read_b128 v[8:11], v3 offset:24576
	v_add_u32_e32 v3, v219, v221
	ds_read_b128 v[236:239], v3 offset:16384
	ds_read_b128 v[240:243], v3 offset:24576
	v_add_u32_e32 v3, v219, v222
	ds_read_b128 v[244:247], v3 offset:16384
	ds_read_b128 v[248:251], v3 offset:24576
	s_add_i32 s27, s25, 63
	s_cmp_lt_i32 s27, s23
	v_add_u32_e32 v3, v219, v223
	s_waitcnt lgkmcnt(5)
	v_mfma_f32_32x32x16_bf16 v[82:97], v[4:7], v[114:117], 0
	s_waitcnt lgkmcnt(4)
	v_mfma_f32_32x32x16_bf16 v[98:113], v[8:11], v[114:117], 0
	ds_read_b128 v[4:7], v3 offset:16384
	ds_read_b128 v[8:11], v3 offset:24576
	v_add_u32_e32 v3, v219, v224
	s_waitcnt lgkmcnt(5)
	v_mfma_f32_32x32x16_bf16 v[82:97], v[236:239], v[118:121], v[82:97]
	s_waitcnt lgkmcnt(4)
	v_mfma_f32_32x32x16_bf16 v[98:113], v[240:243], v[118:121], v[98:113]
	ds_read_b128 v[236:239], v3 offset:16384
	ds_read_b128 v[240:243], v3 offset:24576
	v_add_u32_e32 v3, v219, v225
	s_waitcnt lgkmcnt(5)
	v_mfma_f32_32x32x16_bf16 v[82:97], v[244:247], v[122:125], v[82:97]
	s_waitcnt lgkmcnt(4)
	v_mfma_f32_32x32x16_bf16 v[98:113], v[248:251], v[122:125], v[98:113]
	ds_read_b128 v[244:247], v3 offset:16384
	ds_read_b128 v[248:251], v3 offset:24576
	v_add_u32_e32 v3, v219, v226
	s_waitcnt lgkmcnt(5)
	v_mfma_f32_32x32x16_bf16 v[82:97], v[4:7], v[126:129], v[82:97]
	s_waitcnt lgkmcnt(4)
	v_mfma_f32_32x32x16_bf16 v[98:113], v[8:11], v[126:129], v[98:113]
	ds_read_b128 v[4:7], v3 offset:16384
	ds_read_b128 v[8:11], v3 offset:24576
	v_add_u32_e32 v3, v219, v227
	s_waitcnt lgkmcnt(5)
	v_mfma_f32_32x32x16_bf16 v[82:97], v[236:239], v[130:133], v[82:97]
	s_waitcnt lgkmcnt(4)
	v_mfma_f32_32x32x16_bf16 v[98:113], v[240:243], v[130:133], v[98:113]
	ds_read_b128 v[236:239], v3 offset:16384
	ds_read_b128 v[240:243], v3 offset:24576
	s_waitcnt lgkmcnt(5)
	v_mfma_f32_32x32x16_bf16 v[82:97], v[244:247], v[134:137], v[82:97]
	s_waitcnt lgkmcnt(4)
	v_mfma_f32_32x32x16_bf16 v[98:113], v[248:251], v[134:137], v[98:113]
	s_waitcnt lgkmcnt(3)
	v_mfma_f32_32x32x16_bf16 v[82:97], v[4:7], v[138:141], v[82:97]
	s_waitcnt lgkmcnt(2)
	v_mfma_f32_32x32x16_bf16 v[98:113], v[8:11], v[138:141], v[98:113]
	s_waitcnt lgkmcnt(1)
	v_mfma_f32_32x32x16_bf16 v[82:97], v[236:239], v[142:145], v[82:97]
	s_waitcnt lgkmcnt(0)
	v_mfma_f32_32x32x16_bf16 v[98:113], v[240:243], v[142:145], v[98:113]
	s_cmp_lg_u32 s58, 0
	s_cbranch_scc1 .Lst0_nob2_1
	s_barrier
.Lst0_nob2_1:
	s_add_i32 s27, s25, 63
	s_cmp_lt_i32 s27, s23
	s_cbranch_scc1 .LBB0_717
	v_add_u32_e32 v3, s25, v217
	v_cmp_lt_i32_e32 vcc, v3, v234
	v_add_u32_e32 v4, 32, v3
	s_nop 5
	v_cndmask_b32_e32 v82, v233, v82, vcc
	v_cmp_lt_i32_e32 vcc, v4, v234
	v_add_u32_e32 v4, 1, v3
	s_nop 0
	v_cndmask_b32_e32 v98, v233, v98, vcc
	v_cmp_lt_i32_e32 vcc, v4, v234
	v_add_u32_e32 v4, 33, v3
	s_nop 0
	v_cndmask_b32_e32 v83, v233, v83, vcc
	v_cmp_lt_i32_e32 vcc, v4, v234
	v_add_u32_e32 v4, 2, v3
	s_nop 0
	v_cndmask_b32_e32 v99, v233, v99, vcc
	v_cmp_lt_i32_e32 vcc, v4, v234
	v_add_u32_e32 v4, 34, v3
	s_nop 0
	v_cndmask_b32_e32 v84, v233, v84, vcc
	v_cmp_lt_i32_e32 vcc, v4, v234
	v_add_u32_e32 v4, 3, v3
	s_nop 0
	v_cndmask_b32_e32 v100, v233, v100, vcc
	v_cmp_lt_i32_e32 vcc, v4, v234
	v_add_u32_e32 v4, 35, v3
	s_nop 0
	v_cndmask_b32_e32 v85, v233, v85, vcc
	v_cmp_lt_i32_e32 vcc, v4, v234
	v_add_u32_e32 v4, 8, v3
	s_nop 0
	v_cndmask_b32_e32 v101, v233, v101, vcc
	v_cmp_lt_i32_e32 vcc, v4, v234
	v_add_u32_e32 v4, 40, v3
	s_nop 0
	v_cndmask_b32_e32 v86, v233, v86, vcc
	v_cmp_lt_i32_e32 vcc, v4, v234
	v_add_u32_e32 v4, 9, v3
	s_nop 0
	v_cndmask_b32_e32 v102, v233, v102, vcc
	v_cmp_lt_i32_e32 vcc, v4, v234
	v_add_u32_e32 v4, 41, v3
	s_nop 0
	v_cndmask_b32_e32 v87, v233, v87, vcc
	v_cmp_lt_i32_e32 vcc, v4, v234
	v_add_u32_e32 v4, 10, v3
	s_nop 0
	v_cndmask_b32_e32 v103, v233, v103, vcc
	v_cmp_lt_i32_e32 vcc, v4, v234
	v_add_u32_e32 v4, 42, v3
	s_nop 0
	v_cndmask_b32_e32 v88, v233, v88, vcc
	v_cmp_lt_i32_e32 vcc, v4, v234
	v_add_u32_e32 v4, 11, v3
	s_nop 0
	v_cndmask_b32_e32 v104, v233, v104, vcc
	v_cmp_lt_i32_e32 vcc, v4, v234
	v_add_u32_e32 v4, 43, v3
	s_nop 0
	v_cndmask_b32_e32 v89, v233, v89, vcc
	v_cmp_lt_i32_e32 vcc, v4, v234
	v_add_u32_e32 v4, 16, v3
	s_nop 0
	v_cndmask_b32_e32 v105, v233, v105, vcc
	v_cmp_lt_i32_e32 vcc, v4, v234
	v_add_u32_e32 v4, 48, v3
	s_nop 0
	v_cndmask_b32_e32 v90, v233, v90, vcc
	v_cmp_lt_i32_e32 vcc, v4, v234
	v_add_u32_e32 v4, 17, v3
	s_nop 0
	v_cndmask_b32_e32 v106, v233, v106, vcc
	v_cmp_lt_i32_e32 vcc, v4, v234
	v_add_u32_e32 v4, 49, v3
	s_nop 0
	v_cndmask_b32_e32 v91, v233, v91, vcc
	v_cmp_lt_i32_e32 vcc, v4, v234
	v_add_u32_e32 v4, 18, v3
	s_nop 0
	v_cndmask_b32_e32 v107, v233, v107, vcc
	v_cmp_lt_i32_e32 vcc, v4, v234
	v_add_u32_e32 v4, 50, v3
	s_nop 0
	v_cndmask_b32_e32 v92, v233, v92, vcc
	v_cmp_lt_i32_e32 vcc, v4, v234
	v_add_u32_e32 v4, 19, v3
	s_nop 0
	v_cndmask_b32_e32 v108, v233, v108, vcc
	v_cmp_lt_i32_e32 vcc, v4, v234
	v_add_u32_e32 v4, 51, v3
	s_nop 0
	v_cndmask_b32_e32 v93, v233, v93, vcc
	v_cmp_lt_i32_e32 vcc, v4, v234
	v_add_u32_e32 v4, 24, v3
	s_nop 0
	v_cndmask_b32_e32 v109, v233, v109, vcc
	v_cmp_lt_i32_e32 vcc, v4, v234
	v_add_u32_e32 v4, 56, v3
	s_nop 0
	v_cndmask_b32_e32 v94, v233, v94, vcc
	v_cmp_lt_i32_e32 vcc, v4, v234
	v_add_u32_e32 v4, 25, v3
	s_nop 0
	v_cndmask_b32_e32 v110, v233, v110, vcc
	v_cmp_lt_i32_e32 vcc, v4, v234
	v_add_u32_e32 v4, 57, v3
	s_nop 0
	v_cndmask_b32_e32 v95, v233, v95, vcc
	v_cmp_lt_i32_e32 vcc, v4, v234
	v_add_u32_e32 v4, 26, v3
	s_nop 0
	v_cndmask_b32_e32 v111, v233, v111, vcc
	v_cmp_lt_i32_e32 vcc, v4, v234
	v_add_u32_e32 v4, 58, v3
	s_nop 0
	v_cndmask_b32_e32 v96, v233, v96, vcc
	v_cmp_lt_i32_e32 vcc, v4, v234
	v_add_u32_e32 v4, 27, v3
	v_add_u32_e32 v3, 59, v3
	v_cndmask_b32_e32 v112, v233, v112, vcc
	v_cmp_lt_i32_e32 vcc, v4, v234
	s_nop 1
	v_cndmask_b32_e32 v97, v233, v97, vcc
	v_cmp_lt_i32_e32 vcc, v3, v234
	s_nop 1
	v_cndmask_b32_e32 v113, v233, v113, vcc
.LBB0_717:
	s_nop 10
	v_exp_f32_e32 v3, v98
	v_exp_f32_e32 v4, v82
	v_exp_f32_e32 v98, v112
	v_exp_f32_e32 v6, v99
	v_add_f32_e32 v3, 1.0, v3
	v_add_f32_e32 v5, 1.0, v4
	v_rcp_f32_e32 v4, v3
	v_exp_f32_e32 v3, v83
	v_exp_f32_e32 v99, v97
	v_exp_f32_e32 v16, v104
	v_exp_f32_e32 v82, v105
	v_add_f32_e32 v3, 1.0, v3
	v_rcp_f32_e32 v7, v3
	v_exp_f32_e32 v3, v84
	v_exp_f32_e32 v84, v106
	v_exp_f32_e32 v8, v100
	v_exp_f32_e32 v10, v101
	v_add_f32_e32 v3, 1.0, v3
	v_rcp_f32_e32 v9, v3
	v_exp_f32_e32 v3, v85
	v_exp_f32_e32 v14, v103
	v_exp_f32_e32 v12, v102
	v_add_f32_e32 v84, 1.0, v84
	v_add_f32_e32 v3, 1.0, v3
	v_rcp_f32_e32 v11, v3
	v_exp_f32_e32 v3, v86
	v_exp_f32_e32 v86, v107
	v_rcp_f32_e32 v84, v84
	v_add_f32_e32 v16, 1.0, v16
	v_add_f32_e32 v3, 1.0, v3
	v_rcp_f32_e32 v13, v3
	v_exp_f32_e32 v3, v87
	v_add_f32_e32 v86, 1.0, v86
	v_rcp_f32_e32 v86, v86
	v_add_f32_e32 v82, 1.0, v82
	v_add_f32_e32 v3, 1.0, v3
	v_rcp_f32_e32 v15, v3
	v_exp_f32_e32 v3, v88
	v_exp_f32_e32 v88, v108
	v_add_f32_e32 v8, 1.0, v8
	v_add_f32_e32 v10, 1.0, v10
	v_add_f32_e32 v3, 1.0, v3
	v_rcp_f32_e32 v17, v3
	v_exp_f32_e32 v3, v89
	v_add_f32_e32 v88, 1.0, v88
	v_rcp_f32_e32 v88, v88
	v_add_f32_e32 v14, 1.0, v14
	v_add_f32_e32 v3, 1.0, v3
	v_rcp_f32_e32 v83, v3
	v_exp_f32_e32 v3, v90
	v_exp_f32_e32 v90, v109
	v_rcp_f32_e32 v16, v16
	v_rcp_f32_e32 v82, v82
	v_add_f32_e32 v3, 1.0, v3
	v_rcp_f32_e32 v85, v3
	v_exp_f32_e32 v3, v91
	v_add_f32_e32 v90, 1.0, v90
	v_rcp_f32_e32 v90, v90
	v_add_f32_e32 v6, 1.0, v6
	v_add_f32_e32 v3, 1.0, v3
	v_rcp_f32_e32 v87, v3
	v_exp_f32_e32 v3, v92
	v_exp_f32_e32 v92, v110
	v_rcp_f32_e32 v8, v8
	v_rcp_f32_e32 v10, v10
	v_add_f32_e32 v3, 1.0, v3
	v_rcp_f32_e32 v89, v3
	v_exp_f32_e32 v3, v93
	v_add_f32_e32 v92, 1.0, v92
	v_rcp_f32_e32 v92, v92
	v_add_f32_e32 v12, 1.0, v12
	v_add_f32_e32 v3, 1.0, v3
	v_rcp_f32_e32 v91, v3
	v_exp_f32_e32 v3, v94
	v_exp_f32_e32 v94, v111
	v_rcp_f32_e32 v14, v14
	v_pk_mul_f32 v[214:215], v[88:89], v[90:91]
	v_add_f32_e32 v3, 1.0, v3
	v_rcp_f32_e32 v93, v3
	v_exp_f32_e32 v3, v95
	v_add_f32_e32 v94, 1.0, v94
	v_rcp_f32_e32 v94, v94
	v_pk_mul_f32 v[236:237], v[86:87], v[214:215]
	v_add_f32_e32 v3, 1.0, v3
	v_rcp_f32_e32 v95, v3
	v_exp_f32_e32 v3, v96
	v_add_f32_e32 v96, 1.0, v98
	v_exp_f32_e32 v98, v113
	v_rcp_f32_e32 v96, v96
	v_add_f32_e32 v3, 1.0, v3
	v_rcp_f32_e32 v97, v3
	v_add_f32_e32 v3, 1.0, v98
	v_rcp_f32_e32 v98, v3
	v_add_f32_e32 v3, 1.0, v99
	v_rcp_f32_e32 v99, v3
	v_rcp_f32_e32 v6, v6
	v_rcp_f32_e32 v12, v12
	v_pk_mul_f32 v[238:239], v[84:85], v[236:237]
	v_pk_mul_f32 v[244:245], v[96:97], v[98:99]
	v_rcp_f32_e32 v5, v5
	v_pk_mul_f32 v[246:247], v[94:95], v[244:245]
	v_mov_b32_e32 v240, v238
	v_pk_mul_f32 v[248:249], v[92:93], v[246:247]
	v_pk_mul_f32 v[110:111], v[16:17], v[82:83]
	v_mov_b32_e32 v107, v248
	s_nop 1
	v_permlane32_swap_b32_e32 v248, v107
	v_permlane32_swap_b32_e32 v238, v240
	v_mul_f32_e32 v190, v191, v107
	v_pk_mul_f32 v[100:101], v[8:9], v[10:11]
	v_pk_mul_f32 v[112:113], v[14:15], v[110:111]
	v_cndmask_b32_e64 v250, v191, v190, s[2:3]
	v_mul_f32_e32 v241, v248, v107
	v_mov_b32_e32 v190, v238
	v_pk_mul_f32 v[102:103], v[6:7], v[100:101]
	v_pk_mul_f32 v[206:207], v[12:13], v[112:113]
	v_pk_mul_f32 v[190:191], v[190:191], v[240:241]
	v_pk_mul_f32 v[104:105], v[4:5], v[102:103]
	v_mov_b32_e32 v3, v206
	v_mul_f32_e32 v107, v191, v240
	v_mov_b32_e32 v106, v104
	v_permlane32_swap_b32_e32 v206, v3
	v_cndmask_b32_e64 v238, v191, v107, s[2:3]
	v_pk_mul_f32 v[190:191], v[190:191], v[190:191] op_sel:[0,1] op_sel_hi:[1,0]
	v_permlane32_swap_b32_e32 v104, v106
	v_mul_f32_e32 v107, v190, v3
	v_cndmask_b32_e64 v240, v190, v107, s[2:3]
	v_mul_f32_e32 v253, v206, v3
	v_mov_b32_e32 v252, v104
	v_mov_b32_e32 v107, v190
	v_mov_b32_e32 v242, v239
	v_mov_b32_e32 v243, v249
	v_pk_mul_f32 v[190:191], v[252:253], v[106:107]
	v_permlane32_swap_b32_e32 v239, v242
	v_permlane32_swap_b32_e32 v249, v243
	v_mul_f32_e32 v3, v191, v106
	v_pk_mul_f32 v[106:107], v[190:191], v[190:191] op_sel:[0,1] op_sel_hi:[1,0]
	v_cndmask_b32_e64 v104, v191, v3, s[2:3]
	v_mul_f32_e32 v3, v106, v243
	v_mul_f32_e32 v191, v249, v243
	v_mov_b32_e32 v190, v239
	v_mov_b32_e32 v243, v106
	v_cndmask_b32_e64 v251, v106, v3, s[2:3]
	v_pk_mul_f32 v[106:107], v[190:191], v[242:243]
	v_mov_b32_e32 v108, v105
	v_mov_b32_e32 v109, v207
	v_mul_f32_e32 v3, v107, v242
	v_permlane32_swap_b32_e32 v105, v108
	v_permlane32_swap_b32_e32 v207, v109
	v_cndmask_b32_e64 v239, v107, v3, s[2:3]
	v_pk_mul_f32 v[106:107], v[106:107], v[106:107] op_sel:[0,1] op_sel_hi:[1,0]
	v_mul_f32_e32 v191, v207, v109
	v_mul_f32_e32 v3, v106, v109
	v_mov_b32_e32 v190, v105
	v_mov_b32_e32 v109, v106
	v_cndmask_b32_e64 v241, v106, v3, s[2:3]
	v_pk_mul_f32 v[106:107], v[190:191], v[108:109]
	s_nop 0
	v_mul_f32_e32 v3, v107, v108
	v_cndmask_b32_e64 v105, v107, v3, s[2:3]
	v_mul_f32_e32 v191, v106, v107
	v_pk_mul_f32 v[106:107], v[10:11], v[104:105]
	v_pk_mul_f32 v[100:101], v[100:101], v[104:105]
	v_pk_mul_f32 v[102:103], v[102:103], v[104:105]
	v_pk_fma_f32 v[106:107], v[8:9], v[106:107], v[106:107] neg_lo:[1,0,0] neg_hi:[1,0,0]
	v_pk_fma_f32 v[100:101], v[6:7], v[100:101], v[100:101] neg_lo:[1,0,0] neg_hi:[1,0,0]
	v_pk_mul_f32 v[6:7], v[110:111], v[240:241]
	v_pk_mul_f32 v[8:9], v[112:113], v[240:241]
	v_pk_fma_f32 v[102:103], v[4:5], v[102:103], v[102:103] neg_lo:[1,0,0] neg_hi:[1,0,0]
	v_pk_mul_f32 v[4:5], v[82:83], v[240:241]
	v_pk_fma_f32 v[14:15], v[14:15], v[6:7], v[6:7] neg_lo:[1,0,0] neg_hi:[1,0,0]
	v_pk_fma_f32 v[108:109], v[12:13], v[8:9], v[8:9] neg_lo:[1,0,0] neg_hi:[1,0,0]
	v_pk_mul_f32 v[6:7], v[214:215], v[238:239]
	v_pk_mul_f32 v[8:9], v[236:237], v[238:239]
	v_pk_fma_f32 v[82:83], v[82:83], v[240:241], v[240:241] neg_lo:[1,0,0] neg_hi:[1,0,0]
	v_pk_fma_f32 v[16:17], v[16:17], v[4:5], v[4:5] neg_lo:[1,0,0] neg_hi:[1,0,0]
	v_pk_mul_f32 v[4:5], v[90:91], v[238:239]
	v_pk_fma_f32 v[86:87], v[86:87], v[6:7], v[6:7] neg_lo:[1,0,0] neg_hi:[1,0,0]
	v_pk_fma_f32 v[84:85], v[84:85], v[8:9], v[8:9] neg_lo:[1,0,0] neg_hi:[1,0,0]
	v_pk_mul_f32 v[6:7], v[244:245], v[250:251]
	v_pk_mul_f32 v[8:9], v[246:247], v[250:251]
	v_pk_fma_f32 v[90:91], v[90:91], v[238:239], v[238:239] neg_lo:[1,0,0] neg_hi:[1,0,0]
	v_pk_fma_f32 v[88:89], v[88:89], v[4:5], v[4:5] neg_lo:[1,0,0] neg_hi:[1,0,0]
	v_pk_fma_f32 v[94:95], v[94:95], v[6:7], v[6:7] neg_lo:[1,0,0] neg_hi:[1,0,0]
	v_pk_fma_f32 v[92:93], v[92:93], v[8:9], v[8:9] neg_lo:[1,0,0] neg_hi:[1,0,0]
	s_cmp_lg_u32 s58, 0
	s_cbranch_scc0 .Lst0_tail1
	s_mov_b32 s59, 2
	s_branch .LBB0_718
.Lst0_tail1:
	v_cvt_pk_bf16_f32 v6, v109, v15
	v_cvt_pk_bf16_f32 v8, v85, v87
	v_cvt_pk_bf16_f32 v15, v16, v82
	v_cvt_pk_bf16_f32 v82, v84, v86
	ds_read_b64_tr_b16 v[86:87], v228 offset:0
	v_cvt_pk_bf16_f32 v7, v17, v83
	v_cvt_pk_bf16_f32 v9, v89, v91
	v_cvt_pk_bf16_f32 v83, v88, v90
	ds_read_b64_tr_b16 v[88:89], v228 offset:0x800
	ds_read_b64_tr_b16 v[90:91], v228 offset:0x1000
	v_pk_fma_f32 v[104:105], v[10:11], v[104:105], v[104:105] neg_lo:[1,0,0] neg_hi:[1,0,0]
	v_pk_mul_f32 v[4:5], v[98:99], v[250:251]
	v_cvt_pk_bf16_f32 v10, v93, v95
	v_cvt_pk_bf16_f32 v84, v92, v94
	ds_read_b64_tr_b16 v[92:93], v228 offset:0x1800
	v_pk_fma_f32 v[98:99], v[98:99], v[250:251], v[250:251] neg_lo:[1,0,0] neg_hi:[1,0,0]
	v_pk_fma_f32 v[96:97], v[96:97], v[4:5], v[4:5] neg_lo:[1,0,0] neg_hi:[1,0,0]
	ds_read_b64_tr_b16 v[94:95], v228 offset:0x2000
	v_cvt_pk_bf16_f32 v4, v103, v101
	v_cvt_pk_bf16_f32 v11, v97, v99
	v_cvt_pk_bf16_f32 v85, v96, v98
	ds_read_b64_tr_b16 v[96:97], v228 offset:0x2800
	ds_read_b64_tr_b16 v[98:99], v228 offset:0x3000
	v_cvt_pk_bf16_f32 v12, v102, v100
	ds_read_b64_tr_b16 v[100:101], v228 offset:0x3800
	s_waitcnt lgkmcnt(0)
	v_cvt_pk_bf16_f32 v5, v107, v105
	v_cvt_pk_bf16_f32 v13, v106, v104
	v_cvt_pk_bf16_f32 v14, v108, v14
	v_permlane32_swap_b32_e32 v4, v6
	v_permlane32_swap_b32_e32 v5, v7
	v_permlane32_swap_b32_e32 v8, v10
	v_permlane32_swap_b32_e32 v9, v11
	v_permlane32_swap_b32_e32 v12, v14
	v_permlane32_swap_b32_e32 v13, v15
	v_permlane32_swap_b32_e32 v82, v84
	v_permlane32_swap_b32_e32 v83, v85
	v_mfma_f32_32x32x16_bf16 v[66:81], v[4:7], v[86:89], v[66:81]
	ds_read_b64_tr_b16 v[86:87], v228 offset:0x200
	ds_read_b64_tr_b16 v[88:89], v228 offset:0xa00
	v_mfma_f32_32x32x16_bf16 v[66:81], v[8:11], v[90:93], v[66:81]
	ds_read_b64_tr_b16 v[90:91], v228 offset:0x1200
	ds_read_b64_tr_b16 v[92:93], v228 offset:0x1a00
	v_mfma_f32_32x32x16_bf16 v[66:81], v[12:15], v[94:97], v[66:81]
	ds_read_b64_tr_b16 v[94:95], v228 offset:0x2200
	ds_read_b64_tr_b16 v[96:97], v228 offset:0x2a00
	ds_read_b64_tr_b16 v[102:103], v228 offset:0x3200
	ds_read_b64_tr_b16 v[104:105], v228 offset:0x3a00
	s_waitcnt lgkmcnt(0)
	v_mfma_f32_32x32x16_bf16 v[66:81], v[82:85], v[98:101], v[66:81]
	v_mfma_f32_32x32x16_bf16 v[50:65], v[4:7], v[86:89], v[50:65]
	ds_read_b64_tr_b16 v[86:87], v228 offset:0x400
	ds_read_b64_tr_b16 v[88:89], v228 offset:0xc00
	v_mfma_f32_32x32x16_bf16 v[50:65], v[8:11], v[90:93], v[50:65]
	ds_read_b64_tr_b16 v[90:91], v228 offset:0x1400
	ds_read_b64_tr_b16 v[92:93], v228 offset:0x1c00
	v_mfma_f32_32x32x16_bf16 v[50:65], v[12:15], v[94:97], v[50:65]
	ds_read_b64_tr_b16 v[94:95], v228 offset:0x2400
	ds_read_b64_tr_b16 v[96:97], v228 offset:0x2c00
	ds_read_b64_tr_b16 v[98:99], v228 offset:0x3400
	ds_read_b64_tr_b16 v[100:101], v228 offset:0x3c00
	s_waitcnt lgkmcnt(0)
	v_mfma_f32_32x32x16_bf16 v[50:65], v[82:85], v[102:105], v[50:65]
	v_mfma_f32_32x32x16_bf16 v[34:49], v[4:7], v[86:89], v[34:49]
	ds_read_b64_tr_b16 v[86:87], v228 offset:0x600
	ds_read_b64_tr_b16 v[88:89], v228 offset:0xe00
	v_mfma_f32_32x32x16_bf16 v[34:49], v[8:11], v[90:93], v[34:49]
	ds_read_b64_tr_b16 v[90:91], v228 offset:0x1600
	ds_read_b64_tr_b16 v[92:93], v228 offset:0x1e00
	v_mfma_f32_32x32x16_bf16 v[34:49], v[12:15], v[94:97], v[34:49]
	ds_read_b64_tr_b16 v[94:95], v228 offset:0x2600
	ds_read_b64_tr_b16 v[96:97], v228 offset:0x2e00
	ds_read_b64_tr_b16 v[102:103], v228 offset:0x3600
	ds_read_b64_tr_b16 v[104:105], v228 offset:0x3e00
	s_waitcnt lgkmcnt(0)
	v_mfma_f32_32x32x16_bf16 v[34:49], v[82:85], v[98:101], v[34:49]
	v_mfma_f32_32x32x16_bf16 v[18:33], v[4:7], v[86:89], v[18:33]
	v_mfma_f32_32x32x16_bf16 v[18:33], v[8:11], v[90:93], v[18:33]
	v_mfma_f32_32x32x16_bf16 v[18:33], v[12:15], v[94:97], v[18:33]
	v_mfma_f32_32x32x16_bf16 v[18:33], v[82:85], v[102:105], v[18:33]
	s_cmp_lg_u32 s60, 0
	s_cbranch_scc0 .LBB0_718
	s_cmp_eq_u32 s60, 2
	s_mov_b32 s60, 0
	s_cbranch_scc1 .Lst0_epi
	s_branch .Lst0_ret0

.LBB0_720:
	s_waitcnt lgkmcnt(0)
	s_cmp_ge_u32 s26, s20
	s_barrier
	s_cbranch_scc1 .LBB0_722
	s_add_i32 s30, s6, -1
	s_ashr_i32 s31, s30, 31
	s_lshl_b64 s[30:31], s[30:31], 6
	v_mov_b32_e32 v237, s31
	v_or_b32_e32 v236, s30, v193
	v_lshlrev_b64 v[236:237], 11, v[236:237]
	v_mov_b32_e32 v241, s31
	v_or_b32_e32 v240, s30, v194
	v_lshl_add_u64 v[238:239], v[186:187], 0, v[236:237]
	v_lshlrev_b64 v[240:241], 11, v[240:241]
	v_lshl_add_u64 v[236:237], v[188:189], 0, v[236:237]
	v_lshl_add_u64 v[242:243], v[186:187], 0, v[240:241]
	global_load_dwordx4 v[154:157], v[238:239], off
	global_load_dwordx4 v[162:165], v[242:243], off
	v_lshl_add_u64 v[238:239], v[188:189], 0, v[240:241]
	global_load_dwordx4 v[170:173], v[236:237], off
	global_load_dwordx4 v[174:177], v[238:239], off
.LBB0_722:
	s_add_i32 s6, s6, -2
	s_andn2_b64 vcc, exec, s[28:29]
	s_addk_i32 s25, 0xff80
	s_cbranch_vccnz .LBB0_708
	s_cmp_eq_u32 s59, 2
	s_cbranch_scc0 .Lst0_epi_chk1
	s_mov_b32 s59, 0
	s_mov_b32 s60, 2
	s_branch .Lst0_tail1
.Lst0_epi_chk1:
	s_cmp_eq_u32 s59, 1
	s_cbranch_scc0 .Lst0_epi
	s_mov_b32 s59, 0
	s_mov_b32 s60, 2
	s_branch .Lst0_tail0
.Lst0_epi:
	s_nop 15
	s_nop 7
	s_lshl_b64 s[22:23], s[56:57], 11
	s_add_u32 s6, s92, s22
	s_addc_u32 s22, s93, s23
	s_lshl_b32 s20, s21, 1
	s_add_u32 s20, s6, s20
	s_addc_u32 s21, s22, 0
	v_lshlrev_b32_e32 v4, 1, v216
	v_mov_b32_e32 v5, v2
	v_lshl_add_u64 v[4:5], s[20:21], 0, v[4:5]
	v_lshl_add_u64 v[4:5], v[4:5], 0, v[180:181]
	v_cvt_pk_bf16_f32 v3, v66, s0
	global_store_short v[4:5], v3, off
	v_cvt_pk_bf16_f32 v3, v50, s0
	global_store_short v[4:5], v3, off offset:64
	v_cvt_pk_bf16_f32 v3, v34, s0
	global_store_short v[4:5], v3, off offset:128
	v_cvt_pk_bf16_f32 v3, v18, s0
	global_store_short v[4:5], v3, off offset:192
	v_cvt_pk_bf16_f32 v3, v67, s0
	global_store_short v[4:5], v3, off offset:2048
	v_cvt_pk_bf16_f32 v3, v51, s0
	global_store_short v[4:5], v3, off offset:2112
	v_cvt_pk_bf16_f32 v3, v35, s0
	global_store_short v[4:5], v3, off offset:2176
	v_cvt_pk_bf16_f32 v3, v19, s0
	v_add_co_u32_e32 v6, vcc, s12, v4
	global_store_short v[4:5], v3, off offset:2240
	v_cvt_pk_bf16_f32 v3, v68, s0
	v_addc_co_u32_e32 v7, vcc, 0, v5, vcc
	global_store_short v[6:7], v3, off
	v_cvt_pk_bf16_f32 v3, v52, s0
	global_store_short v[6:7], v3, off offset:64
	v_cvt_pk_bf16_f32 v3, v36, s0
	global_store_short v[6:7], v3, off offset:128
	v_cvt_pk_bf16_f32 v3, v20, s0
	global_store_short v[6:7], v3, off offset:192
	v_cvt_pk_bf16_f32 v3, v69, s0
	global_store_short v[6:7], v3, off offset:2048
	v_cvt_pk_bf16_f32 v3, v53, s0
	global_store_short v[6:7], v3, off offset:2112
	v_cvt_pk_bf16_f32 v3, v37, s0
	global_store_short v[6:7], v3, off offset:2176
	v_cvt_pk_bf16_f32 v3, v21, s0
	global_store_short v[6:7], v3, off offset:2240
	v_add_co_u32_e32 v6, vcc, s13, v4
	v_cvt_pk_bf16_f32 v3, v70, s0
	s_nop 0
	v_addc_co_u32_e32 v7, vcc, 0, v5, vcc
	v_add_co_u32_e32 v8, vcc, s16, v4
	s_add_i32 s19, s19, s9
	s_nop 0
	v_addc_co_u32_e32 v9, vcc, 0, v5, vcc
	global_store_short v[8:9], v3, off offset:-4096
	v_cvt_pk_bf16_f32 v3, v54, s0
	global_store_short v[6:7], v3, off offset:64
	v_cvt_pk_bf16_f32 v3, v38, s0
	global_store_short v[6:7], v3, off offset:128
	v_cvt_pk_bf16_f32 v3, v22, s0
	global_store_short v[6:7], v3, off offset:192
	v_cvt_pk_bf16_f32 v3, v71, s0
	global_store_short v[6:7], v3, off offset:2048
	v_cvt_pk_bf16_f32 v3, v55, s0
	global_store_short v[6:7], v3, off offset:2112
	v_cvt_pk_bf16_f32 v3, v39, s0
	global_store_short v[6:7], v3, off offset:2176
	v_cvt_pk_bf16_f32 v3, v23, s0
	global_store_short v[6:7], v3, off offset:2240
	v_cvt_pk_bf16_f32 v3, v72, s0
	global_store_short v[8:9], v3, off
	v_cvt_pk_bf16_f32 v3, v56, s0
	global_store_short v[8:9], v3, off offset:64
	v_cvt_pk_bf16_f32 v3, v40, s0
	global_store_short v[8:9], v3, off offset:128
	v_cvt_pk_bf16_f32 v3, v24, s0
	global_store_short v[8:9], v3, off offset:192
	v_cvt_pk_bf16_f32 v3, v73, s0
	global_store_short v[8:9], v3, off offset:2048
	v_cvt_pk_bf16_f32 v3, v57, s0
	global_store_short v[8:9], v3, off offset:2112
	v_cvt_pk_bf16_f32 v3, v41, s0
	v_add_co_u32_e32 v6, vcc, s10, v4
	global_store_short v[8:9], v3, off offset:2176
	v_cvt_pk_bf16_f32 v3, v25, s0
	v_addc_co_u32_e32 v7, vcc, 0, v5, vcc
	global_store_short v[8:9], v3, off offset:2240
	v_add_co_u32_e32 v8, vcc, s17, v4
	v_cvt_pk_bf16_f32 v3, v74, s0
	s_nop 0
	v_addc_co_u32_e32 v9, vcc, 0, v5, vcc
	global_store_short v[8:9], v3, off offset:-4096
	v_cvt_pk_bf16_f32 v3, v58, s0
	global_store_short v[6:7], v3, off offset:64
	v_cvt_pk_bf16_f32 v3, v42, s0
	global_store_short v[6:7], v3, off offset:128
	v_cvt_pk_bf16_f32 v3, v26, s0
	global_store_short v[6:7], v3, off offset:192
	v_cvt_pk_bf16_f32 v3, v75, s0
	global_store_short v[6:7], v3, off offset:2048
	v_cvt_pk_bf16_f32 v3, v59, s0
	global_store_short v[6:7], v3, off offset:2112
	v_cvt_pk_bf16_f32 v3, v43, s0
	global_store_short v[6:7], v3, off offset:2176
	v_cvt_pk_bf16_f32 v3, v27, s0
	global_store_short v[6:7], v3, off offset:2240
	v_cvt_pk_bf16_f32 v3, v76, s0
	global_store_short v[8:9], v3, off
	v_cvt_pk_bf16_f32 v3, v60, s0
	global_store_short v[8:9], v3, off offset:64
	v_cvt_pk_bf16_f32 v3, v44, s0
	global_store_short v[8:9], v3, off offset:128
	v_cvt_pk_bf16_f32 v3, v28, s0
	global_store_short v[8:9], v3, off offset:192
	v_cvt_pk_bf16_f32 v3, v77, s0
	global_store_short v[8:9], v3, off offset:2048
	v_cvt_pk_bf16_f32 v3, v61, s0
	v_add_co_u32_e32 v6, vcc, s11, v4
	global_store_short v[8:9], v3, off offset:2112
	v_cvt_pk_bf16_f32 v3, v45, s0
	v_addc_co_u32_e32 v7, vcc, 0, v5, vcc
	global_store_short v[8:9], v3, off offset:2176
	v_cvt_pk_bf16_f32 v3, v29, s0
	v_add_co_u32_e32 v4, vcc, s18, v4
	global_store_short v[8:9], v3, off offset:2240
	v_cvt_pk_bf16_f32 v3, v78, s0
	v_addc_co_u32_e32 v5, vcc, 0, v5, vcc
	global_store_short v[4:5], v3, off offset:-4096
	v_cvt_pk_bf16_f32 v3, v62, s0
	global_store_short v[6:7], v3, off offset:64
	v_cvt_pk_bf16_f32 v3, v46, s0
	global_store_short v[6:7], v3, off offset:128
	v_cvt_pk_bf16_f32 v3, v30, s0
	global_store_short v[6:7], v3, off offset:192
	v_cvt_pk_bf16_f32 v3, v79, s0
	global_store_short v[6:7], v3, off offset:2048
	v_cvt_pk_bf16_f32 v3, v63, s0
	global_store_short v[6:7], v3, off offset:2112
	v_cvt_pk_bf16_f32 v3, v47, s0
	global_store_short v[6:7], v3, off offset:2176
	v_cvt_pk_bf16_f32 v3, v31, s0
	global_store_short v[6:7], v3, off offset:2240
	v_cvt_pk_bf16_f32 v3, v80, s0
	global_store_short v[4:5], v3, off
	v_cvt_pk_bf16_f32 v3, v64, s0
	global_store_short v[4:5], v3, off offset:64
	v_cvt_pk_bf16_f32 v3, v48, s0
	global_store_short v[4:5], v3, off offset:128
	v_cvt_pk_bf16_f32 v3, v32, s0
	global_store_short v[4:5], v3, off offset:192
	v_cvt_pk_bf16_f32 v3, v81, s0
	global_store_short v[4:5], v3, off offset:2048
	v_cvt_pk_bf16_f32 v3, v65, s0
	global_store_short v[4:5], v3, off offset:2112
	v_cvt_pk_bf16_f32 v3, v49, s0
	global_store_short v[4:5], v3, off offset:2176
	v_cvt_pk_bf16_f32 v3, v33, s0
	s_cmpk_gt_i32 s19, 0xff
	global_store_short v[4:5], v3, off offset:2240
	s_cbranch_scc0 .LBB0_707

.LBB0_2275:
	v_readfirstlane_b32 s58, v0
	s_nop 3
	s_bfe_u32 s58, s58, 0x10008
	s_mov_b32 s59, 0
	s_mov_b32 s60, 0
	s_ashr_i32 s31, s23, 4
	s_sub_i32 s6, 15, s31
	s_bfe_u32 s26, s23, 0x10003
	v_readfirstlane_b32 s20, v0
	s_lshl_b32 s29, s6, 8
	s_lshl_b32 s24, s6, 2
	s_lshl_b32 s6, s26, 12
	s_lshr_b32 s20, s20, 1
	s_add_i32 s6, s29, s6
	s_and_b32 s30, s20, 0x7fffffe0
	s_add_u32 s20, s30, s6
	s_addc_u32 s21, 0, 0
	s_lshl_b32 s6, s23, 7
	s_and_b32 s25, s6, 0x380
	s_lshl_b32 s6, s25, 1
	s_add_i32 s28, s24, 4
	s_lshl_b32 s33, s26, 23
	v_readlane_b32 s26, v255, 0
	s_add_u32 s26, s26, s33
	v_readlane_b32 s27, v255, 1
	s_addc_u32 s27, s27, 0
	s_add_u32 s26, s26, s6
	s_addc_u32 s27, s27, 0
	v_lshl_add_u64 v[186:187], s[26:27], 0, v[184:185]
	v_readlane_b32 s26, v254, 56
	v_mov_b32_e32 v5, s21
	v_or_b32_e32 v4, s20, v216
	v_readlane_b32 s34, v254, 54
	v_readlane_b32 s27, v254, 57
	s_add_u32 s26, s26, s33
	v_lshlrev_b64 v[4:5], 11, v[4:5]
	v_readlane_b32 s35, v254, 55
	s_addc_u32 s27, s27, 0
	s_add_u32 s26, s26, s6
	v_lshl_add_u64 v[4:5], s[34:35], 0, v[4:5]
	s_waitcnt vmcnt(11)
	v_lshl_add_u64 v[20:21], v[4:5], 0, s[6:7]
	s_addc_u32 s27, s27, 0
	s_or_b32 s6, s24, 3
	v_lshl_add_u64 v[188:189], s[26:27], 0, v[184:185]
	s_lshl_b64 s[26:27], s[6:7], 6
	v_mov_b32_e32 v5, s27
	v_or_b32_e32 v4, s26, v193
	v_mov_b32_e32 v7, s27
	v_or_b32_e32 v6, s26, v194
	v_lshlrev_b64 v[12:13], 11, v[4:5]
	v_lshlrev_b64 v[14:15], 11, v[6:7]
	v_lshl_add_u64 v[4:5], v[186:187], 0, v[12:13]
	v_lshl_add_u64 v[8:9], v[186:187], 0, v[14:15]
	v_lshl_add_u64 v[12:13], v[188:189], 0, v[12:13]
	v_lshl_add_u64 v[16:17], v[188:189], 0, v[14:15]
	global_load_dwordx4 v[4:7], v[4:5], off
	s_nop 0
	global_load_dwordx4 v[8:11], v[8:9], off
	s_nop 0
	global_load_dwordx4 v[12:15], v[12:13], off
	s_nop 0
	global_load_dwordx4 v[16:19], v[16:17], off
	s_or_b32 s6, s24, 2
	v_lshl_add_u64 v[20:21], v[20:21], 0, v[182:183]
	s_lshl_b64 s[26:27], s[6:7], 6
	s_or_b32 s6, s24, 1
	global_load_dwordx4 v[114:117], v[20:21], off
	global_load_dwordx4 v[118:121], v[20:21], off offset:32
	global_load_dwordx4 v[122:125], v[20:21], off offset:64
	global_load_dwordx4 v[126:129], v[20:21], off offset:96
	s_waitcnt lgkmcnt(0)
	global_load_dwordx4 v[130:133], v[20:21], off offset:128
	global_load_dwordx4 v[134:137], v[20:21], off offset:160
	global_load_dwordx4 v[138:141], v[20:21], off offset:192
	global_load_dwordx4 v[142:145], v[20:21], off offset:224
	v_mov_b32_e32 v21, s27
	v_or_b32_e32 v20, s26, v193
	s_waitcnt vmcnt(22)
	v_mov_b32_e32 v23, s27
	v_or_b32_e32 v22, s26, v194
	s_lshl_b64 s[26:27], s[6:7], 6
	v_lshlrev_b64 v[20:21], 11, v[20:21]
	v_mov_b32_e32 v25, s27
	v_or_b32_e32 v24, s26, v193
	s_waitcnt vmcnt(21)
	v_mov_b32_e32 v27, s27
	v_or_b32_e32 v26, s26, v194
	v_lshlrev_b64 v[22:23], 11, v[22:23]
	v_lshl_add_u64 v[28:29], v[186:187], 0, v[20:21]
	v_lshlrev_b64 v[24:25], 11, v[24:25]
	v_lshlrev_b64 v[26:27], 11, v[26:27]
	s_waitcnt vmcnt(20)
	v_lshl_add_u64 v[30:31], v[186:187], 0, v[22:23]
	v_lshl_add_u64 v[20:21], v[188:189], 0, v[20:21]
	v_lshl_add_u64 v[22:23], v[188:189], 0, v[22:23]
	v_lshl_add_u64 v[32:33], v[186:187], 0, v[24:25]
	s_waitcnt vmcnt(19)
	v_lshl_add_u64 v[34:35], v[186:187], 0, v[26:27]
	v_lshl_add_u64 v[24:25], v[188:189], 0, v[24:25]
	v_lshl_add_u64 v[26:27], v[188:189], 0, v[26:27]
	s_add_i32 s29, s30, s29
	s_lshl_b32 s6, s31, 8
	v_mov_b32_e32 v3, v2
	v_or_b32_e32 v234, s29, v216
	s_or_b32 s30, s29, 31
	s_sub_i32 s31, 0xf80, s6
	v_mov_b32_e32 v191, 1.0
	s_mov_b32 s6, s24
	s_mov_b32 s33, s7
	s_waitcnt vmcnt(11)
	ds_write_b128 v229, v[4:7]
	s_waitcnt vmcnt(10)
	ds_write_b128 v230, v[8:11]
	s_waitcnt vmcnt(9)
	ds_write_b128 v231, v[12:15] offset:32768
	s_waitcnt vmcnt(8)
	ds_write_b128 v232, v[16:19] offset:32768
	s_waitcnt lgkmcnt(0)
	s_barrier
	global_load_dwordx4 v[146:149], v[28:29], off
	global_load_dwordx4 v[150:153], v[30:31], off
	global_load_dwordx4 v[158:161], v[20:21], off
	global_load_dwordx4 v[166:169], v[22:23], off
	global_load_dwordx4 v[154:157], v[32:33], off
	global_load_dwordx4 v[162:165], v[34:35], off
	global_load_dwordx4 v[170:173], v[24:25], off
	global_load_dwordx4 v[174:177], v[26:27], off
	v_mov_b32_e32 v16, v2
	v_mov_b32_e32 v17, v2
	v_mov_b32_e32 v4, v2
	v_mov_b32_e32 v5, v2
	v_mov_b32_e32 v6, v2
	v_mov_b32_e32 v7, v2
	v_mov_b32_e32 v8, v2
	v_mov_b32_e32 v9, v2
	v_mov_b32_e32 v10, v2
	v_mov_b32_e32 v11, v2
	v_mov_b32_e32 v12, v2
	v_mov_b32_e32 v13, v2
	v_mov_b32_e32 v14, v2
	v_mov_b32_e32 v15, v2
	v_mov_b64_e32 v[32:33], v[16:17]
	v_mov_b64_e32 v[48:49], v[16:17]
	v_mov_b64_e32 v[64:65], v[16:17]
	v_mov_b64_e32 v[80:81], v[16:17]
	v_mov_b64_e32 v[30:31], v[14:15]
	v_mov_b64_e32 v[28:29], v[12:13]
	v_mov_b64_e32 v[26:27], v[10:11]
	v_mov_b64_e32 v[24:25], v[8:9]
	v_mov_b64_e32 v[22:23], v[6:7]
	v_mov_b64_e32 v[20:21], v[4:5]
	v_mov_b64_e32 v[18:19], v[2:3]
	v_mov_b64_e32 v[46:47], v[14:15]
	v_mov_b64_e32 v[44:45], v[12:13]
	v_mov_b64_e32 v[42:43], v[10:11]
	v_mov_b64_e32 v[40:41], v[8:9]
	v_mov_b64_e32 v[38:39], v[6:7]
	v_mov_b64_e32 v[36:37], v[4:5]
	v_mov_b64_e32 v[34:35], v[2:3]
	v_mov_b64_e32 v[62:63], v[14:15]
	v_mov_b64_e32 v[60:61], v[12:13]
	v_mov_b64_e32 v[58:59], v[10:11]
	v_mov_b64_e32 v[56:57], v[8:9]
	v_mov_b64_e32 v[54:55], v[6:7]
	v_mov_b64_e32 v[52:53], v[4:5]
	v_mov_b64_e32 v[50:51], v[2:3]
	v_mov_b64_e32 v[78:79], v[14:15]
	v_mov_b64_e32 v[76:77], v[12:13]
	v_mov_b64_e32 v[74:75], v[10:11]
	v_mov_b64_e32 v[72:73], v[8:9]
	v_mov_b64_e32 v[70:71], v[6:7]
	v_mov_b64_e32 v[68:69], v[4:5]
	v_mov_b64_e32 v[66:67], v[2:3]
	s_add_i32 s26, s31, 64
	s_cmp_ge_i32 s26, s30
	s_cbranch_scc1 .Lst1_skip0
	s_branch .Lst1_b0

.LBB0_2277:
	v_add_u32_e32 v3, v219, v220
	ds_read_b128 v[4:7], v3
	ds_read_b128 v[8:11], v3 offset:8192
	v_add_u32_e32 v3, v219, v221
	ds_read_b128 v[236:239], v3
	ds_read_b128 v[240:243], v3 offset:8192
	v_add_u32_e32 v3, v219, v222
	ds_read_b128 v[244:247], v3
	ds_read_b128 v[248:251], v3 offset:8192
	s_add_i32 s26, s31, 0x7f
	s_cmp_lt_i32 s26, s29
	v_add_u32_e32 v3, v219, v223
	s_waitcnt vmcnt(15) lgkmcnt(5)
	v_mfma_f32_32x32x16_bf16 v[82:97], v[4:7], v[114:117], 0
	s_waitcnt lgkmcnt(4)
	v_mfma_f32_32x32x16_bf16 v[98:113], v[8:11], v[114:117], 0
	ds_read_b128 v[4:7], v3
	ds_read_b128 v[8:11], v3 offset:8192
	v_add_u32_e32 v3, v219, v224
	s_waitcnt vmcnt(14) lgkmcnt(5)
	v_mfma_f32_32x32x16_bf16 v[82:97], v[236:239], v[118:121], v[82:97]
	s_waitcnt lgkmcnt(4)
	v_mfma_f32_32x32x16_bf16 v[98:113], v[240:243], v[118:121], v[98:113]
	ds_read_b128 v[236:239], v3
	ds_read_b128 v[240:243], v3 offset:8192
	v_add_u32_e32 v3, v219, v225
	s_waitcnt vmcnt(13) lgkmcnt(5)
	v_mfma_f32_32x32x16_bf16 v[82:97], v[244:247], v[122:125], v[82:97]
	s_waitcnt lgkmcnt(4)
	v_mfma_f32_32x32x16_bf16 v[98:113], v[248:251], v[122:125], v[98:113]
	ds_read_b128 v[244:247], v3
	ds_read_b128 v[248:251], v3 offset:8192
	v_add_u32_e32 v3, v219, v226
	s_waitcnt vmcnt(12) lgkmcnt(5)
	v_mfma_f32_32x32x16_bf16 v[82:97], v[4:7], v[126:129], v[82:97]
	s_waitcnt lgkmcnt(4)
	v_mfma_f32_32x32x16_bf16 v[98:113], v[8:11], v[126:129], v[98:113]
	ds_read_b128 v[4:7], v3
	ds_read_b128 v[8:11], v3 offset:8192
	v_add_u32_e32 v3, v219, v227
	s_waitcnt vmcnt(11) lgkmcnt(5)
	v_mfma_f32_32x32x16_bf16 v[82:97], v[236:239], v[130:133], v[82:97]
	s_waitcnt lgkmcnt(4)
	v_mfma_f32_32x32x16_bf16 v[98:113], v[240:243], v[130:133], v[98:113]
	ds_read_b128 v[236:239], v3
	ds_read_b128 v[240:243], v3 offset:8192
	s_waitcnt vmcnt(10) lgkmcnt(5)
	v_mfma_f32_32x32x16_bf16 v[82:97], v[244:247], v[134:137], v[82:97]
	s_waitcnt lgkmcnt(4)
	v_mfma_f32_32x32x16_bf16 v[98:113], v[248:251], v[134:137], v[98:113]
	s_waitcnt vmcnt(9) lgkmcnt(3)
	v_mfma_f32_32x32x16_bf16 v[82:97], v[4:7], v[138:141], v[82:97]
	s_waitcnt lgkmcnt(2)
	v_mfma_f32_32x32x16_bf16 v[98:113], v[8:11], v[138:141], v[98:113]
	s_waitcnt vmcnt(8) lgkmcnt(1)
	v_mfma_f32_32x32x16_bf16 v[82:97], v[236:239], v[142:145], v[82:97]
	s_waitcnt lgkmcnt(0)
	v_mfma_f32_32x32x16_bf16 v[98:113], v[240:243], v[142:145], v[98:113]
	s_cmp_lg_u32 s58, 0
	s_cbranch_scc1 .Lst1_nob2_0
	s_barrier
.Lst1_nob2_0:
	s_add_i32 s26, s31, 0x7f
	s_cmp_lt_i32 s26, s29
	s_cbranch_scc1 .LBB0_2279
	v_add_u32_e32 v3, s31, v217
	v_add_u32_e32 v4, 64, v3
	v_cmp_lt_i32_e32 vcc, v4, v234
	v_add_u32_e32 v4, 0x60, v3
	s_nop 4
	v_cndmask_b32_e32 v82, v233, v82, vcc
	v_cmp_lt_i32_e32 vcc, v4, v234
	v_add_u32_e32 v4, 0x41, v3
	s_nop 0
	v_cndmask_b32_e32 v98, v233, v98, vcc
	v_cmp_lt_i32_e32 vcc, v4, v234
	v_add_u32_e32 v4, 0x61, v3
	s_nop 0
	v_cndmask_b32_e32 v83, v233, v83, vcc
	v_cmp_lt_i32_e32 vcc, v4, v234
	v_add_u32_e32 v4, 0x42, v3
	s_nop 0
	v_cndmask_b32_e32 v99, v233, v99, vcc
	v_cmp_lt_i32_e32 vcc, v4, v234
	v_add_u32_e32 v4, 0x62, v3
	s_nop 0
	v_cndmask_b32_e32 v84, v233, v84, vcc
	v_cmp_lt_i32_e32 vcc, v4, v234
	v_add_u32_e32 v4, 0x43, v3
	s_nop 0
	v_cndmask_b32_e32 v100, v233, v100, vcc
	v_cmp_lt_i32_e32 vcc, v4, v234
	v_add_u32_e32 v4, 0x63, v3
	s_nop 0
	v_cndmask_b32_e32 v85, v233, v85, vcc
	v_cmp_lt_i32_e32 vcc, v4, v234
	v_add_u32_e32 v4, 0x48, v3
	s_nop 0
	v_cndmask_b32_e32 v101, v233, v101, vcc
	v_cmp_lt_i32_e32 vcc, v4, v234
	v_add_u32_e32 v4, 0x68, v3
	s_nop 0
	v_cndmask_b32_e32 v86, v233, v86, vcc
	v_cmp_lt_i32_e32 vcc, v4, v234
	v_add_u32_e32 v4, 0x49, v3
	s_nop 0
	v_cndmask_b32_e32 v102, v233, v102, vcc
	v_cmp_lt_i32_e32 vcc, v4, v234
	v_add_u32_e32 v4, 0x69, v3
	s_nop 0
	v_cndmask_b32_e32 v87, v233, v87, vcc
	v_cmp_lt_i32_e32 vcc, v4, v234
	v_add_u32_e32 v4, 0x4a, v3
	s_nop 0
	v_cndmask_b32_e32 v103, v233, v103, vcc
	v_cmp_lt_i32_e32 vcc, v4, v234
	v_add_u32_e32 v4, 0x6a, v3
	s_nop 0
	v_cndmask_b32_e32 v88, v233, v88, vcc
	v_cmp_lt_i32_e32 vcc, v4, v234
	v_add_u32_e32 v4, 0x4b, v3
	s_nop 0
	v_cndmask_b32_e32 v104, v233, v104, vcc
	v_cmp_lt_i32_e32 vcc, v4, v234
	v_add_u32_e32 v4, 0x6b, v3
	s_nop 0
	v_cndmask_b32_e32 v89, v233, v89, vcc
	v_cmp_lt_i32_e32 vcc, v4, v234
	v_add_u32_e32 v4, 0x50, v3
	s_nop 0
	v_cndmask_b32_e32 v105, v233, v105, vcc
	v_cmp_lt_i32_e32 vcc, v4, v234
	v_add_u32_e32 v4, 0x70, v3
	s_nop 0
	v_cndmask_b32_e32 v90, v233, v90, vcc
	v_cmp_lt_i32_e32 vcc, v4, v234
	v_add_u32_e32 v4, 0x51, v3
	s_nop 0
	v_cndmask_b32_e32 v106, v233, v106, vcc
	v_cmp_lt_i32_e32 vcc, v4, v234
	v_add_u32_e32 v4, 0x71, v3
	s_nop 0
	v_cndmask_b32_e32 v91, v233, v91, vcc
	v_cmp_lt_i32_e32 vcc, v4, v234
	v_add_u32_e32 v4, 0x52, v3
	s_nop 0
	v_cndmask_b32_e32 v107, v233, v107, vcc
	v_cmp_lt_i32_e32 vcc, v4, v234
	v_add_u32_e32 v4, 0x72, v3
	s_nop 0
	v_cndmask_b32_e32 v92, v233, v92, vcc
	v_cmp_lt_i32_e32 vcc, v4, v234
	v_add_u32_e32 v4, 0x53, v3
	s_nop 0
	v_cndmask_b32_e32 v108, v233, v108, vcc
	v_cmp_lt_i32_e32 vcc, v4, v234
	v_add_u32_e32 v4, 0x73, v3
	s_nop 0
	v_cndmask_b32_e32 v93, v233, v93, vcc
	v_cmp_lt_i32_e32 vcc, v4, v234
	v_add_u32_e32 v4, 0x58, v3
	s_nop 0
	v_cndmask_b32_e32 v109, v233, v109, vcc
	v_cmp_lt_i32_e32 vcc, v4, v234
	v_add_u32_e32 v4, 0x78, v3
	s_nop 0
	v_cndmask_b32_e32 v94, v233, v94, vcc
	v_cmp_lt_i32_e32 vcc, v4, v234
	v_add_u32_e32 v4, 0x59, v3
	s_nop 0
	v_cndmask_b32_e32 v110, v233, v110, vcc
	v_cmp_lt_i32_e32 vcc, v4, v234
	v_add_u32_e32 v4, 0x79, v3
	s_nop 0
	v_cndmask_b32_e32 v95, v233, v95, vcc
	v_cmp_lt_i32_e32 vcc, v4, v234
	v_add_u32_e32 v4, 0x5a, v3
	s_nop 0
	v_cndmask_b32_e32 v111, v233, v111, vcc
	v_cmp_lt_i32_e32 vcc, v4, v234
	v_add_u32_e32 v4, 0x7a, v3
	s_nop 0
	v_cndmask_b32_e32 v96, v233, v96, vcc
	v_cmp_lt_i32_e32 vcc, v4, v234
	v_add_u32_e32 v4, 0x5b, v3
	v_add_u32_e32 v3, 0x7b, v3
	v_cndmask_b32_e32 v112, v233, v112, vcc
	v_cmp_lt_i32_e32 vcc, v4, v234
	s_nop 1
	v_cndmask_b32_e32 v97, v233, v97, vcc
	v_cmp_lt_i32_e32 vcc, v3, v234
	s_nop 1
	v_cndmask_b32_e32 v113, v233, v113, vcc

.LBB0_2280:
	s_waitcnt vmcnt(3)
	ds_write_b128 v229, v[146:149] offset:16384
	s_waitcnt vmcnt(2)
	ds_write_b128 v230, v[150:153] offset:16384
	s_waitcnt vmcnt(1)
	ds_write_b128 v231, v[158:161] offset:49152
	s_waitcnt vmcnt(0)
	ds_write_b128 v232, v[166:169] offset:49152
	s_waitcnt lgkmcnt(0)
	s_cmp_gt_u32 s33, s24
	s_barrier
	s_cbranch_scc1 .LBB0_2282
	s_lshl_b64 s[26:27], s[6:7], 6
	v_mov_b32_e32 v237, s27
	v_or_b32_e32 v236, s26, v193
	v_lshlrev_b64 v[236:237], 11, v[236:237]
	v_mov_b32_e32 v241, s27
	v_or_b32_e32 v240, s26, v194
	v_lshl_add_u64 v[238:239], v[186:187], 0, v[236:237]
	v_lshlrev_b64 v[240:241], 11, v[240:241]
	v_lshl_add_u64 v[236:237], v[188:189], 0, v[236:237]
	v_lshl_add_u64 v[242:243], v[186:187], 0, v[240:241]
	global_load_dwordx4 v[146:149], v[238:239], off
	global_load_dwordx4 v[150:153], v[242:243], off
	v_lshl_add_u64 v[238:239], v[188:189], 0, v[240:241]
	global_load_dwordx4 v[158:161], v[236:237], off
	global_load_dwordx4 v[166:169], v[238:239], off
.LBB0_2282:
	s_cmp_ge_i32 s31, s30
	s_cbranch_scc1 .Lst1_skip1
	s_cmp_lg_u32 s58, 0
	s_cbranch_scc1 .Lst1_pre1
.Lst1_qk1:
	v_add_u32_e32 v3, v219, v220
	ds_read_b128 v[4:7], v3 offset:16384
	ds_read_b128 v[8:11], v3 offset:24576
	v_add_u32_e32 v3, v219, v221
	ds_read_b128 v[236:239], v3 offset:16384
	ds_read_b128 v[240:243], v3 offset:24576
	v_add_u32_e32 v3, v219, v222
	ds_read_b128 v[244:247], v3 offset:16384
	ds_read_b128 v[248:251], v3 offset:24576
	s_add_i32 s26, s31, 63
	s_cmp_lt_i32 s26, s29
	v_add_u32_e32 v3, v219, v223
	s_waitcnt lgkmcnt(5)
	v_mfma_f32_32x32x16_bf16 v[82:97], v[4:7], v[114:117], 0
	s_waitcnt lgkmcnt(4)
	v_mfma_f32_32x32x16_bf16 v[98:113], v[8:11], v[114:117], 0
	ds_read_b128 v[4:7], v3 offset:16384
	ds_read_b128 v[8:11], v3 offset:24576
	v_add_u32_e32 v3, v219, v224
	s_waitcnt lgkmcnt(5)
	v_mfma_f32_32x32x16_bf16 v[82:97], v[236:239], v[118:121], v[82:97]
	s_waitcnt lgkmcnt(4)
	v_mfma_f32_32x32x16_bf16 v[98:113], v[240:243], v[118:121], v[98:113]
	ds_read_b128 v[236:239], v3 offset:16384
	ds_read_b128 v[240:243], v3 offset:24576
	v_add_u32_e32 v3, v219, v225
	s_waitcnt lgkmcnt(5)
	v_mfma_f32_32x32x16_bf16 v[82:97], v[244:247], v[122:125], v[82:97]
	s_waitcnt lgkmcnt(4)
	v_mfma_f32_32x32x16_bf16 v[98:113], v[248:251], v[122:125], v[98:113]
	ds_read_b128 v[244:247], v3 offset:16384
	ds_read_b128 v[248:251], v3 offset:24576
	v_add_u32_e32 v3, v219, v226
	s_waitcnt lgkmcnt(5)
	v_mfma_f32_32x32x16_bf16 v[82:97], v[4:7], v[126:129], v[82:97]
	s_waitcnt lgkmcnt(4)
	v_mfma_f32_32x32x16_bf16 v[98:113], v[8:11], v[126:129], v[98:113]
	ds_read_b128 v[4:7], v3 offset:16384
	ds_read_b128 v[8:11], v3 offset:24576
	v_add_u32_e32 v3, v219, v227
	s_waitcnt lgkmcnt(5)
	v_mfma_f32_32x32x16_bf16 v[82:97], v[236:239], v[130:133], v[82:97]
	s_waitcnt lgkmcnt(4)
	v_mfma_f32_32x32x16_bf16 v[98:113], v[240:243], v[130:133], v[98:113]
	ds_read_b128 v[236:239], v3 offset:16384
	ds_read_b128 v[240:243], v3 offset:24576
	s_waitcnt lgkmcnt(5)
	v_mfma_f32_32x32x16_bf16 v[82:97], v[244:247], v[134:137], v[82:97]
	s_waitcnt lgkmcnt(4)
	v_mfma_f32_32x32x16_bf16 v[98:113], v[248:251], v[134:137], v[98:113]
	s_waitcnt lgkmcnt(3)
	v_mfma_f32_32x32x16_bf16 v[82:97], v[4:7], v[138:141], v[82:97]
	s_waitcnt lgkmcnt(2)
	v_mfma_f32_32x32x16_bf16 v[98:113], v[8:11], v[138:141], v[98:113]
	s_waitcnt lgkmcnt(1)
	v_mfma_f32_32x32x16_bf16 v[82:97], v[236:239], v[142:145], v[82:97]
	s_waitcnt lgkmcnt(0)
	v_mfma_f32_32x32x16_bf16 v[98:113], v[240:243], v[142:145], v[98:113]
	s_cmp_lg_u32 s58, 0
	s_cbranch_scc1 .Lst1_nob2_1
	s_barrier
.Lst1_nob2_1:
	s_add_i32 s26, s31, 63
	s_cmp_lt_i32 s26, s29
	s_cbranch_scc1 .LBB0_2285
	v_add_u32_e32 v3, s31, v217
	v_cmp_lt_i32_e32 vcc, v3, v234
	v_add_u32_e32 v4, 32, v3
	s_nop 5
	v_cndmask_b32_e32 v82, v233, v82, vcc
	v_cmp_lt_i32_e32 vcc, v4, v234
	v_add_u32_e32 v4, 1, v3
	s_nop 0
	v_cndmask_b32_e32 v98, v233, v98, vcc
	v_cmp_lt_i32_e32 vcc, v4, v234
	v_add_u32_e32 v4, 33, v3
	s_nop 0
	v_cndmask_b32_e32 v83, v233, v83, vcc
	v_cmp_lt_i32_e32 vcc, v4, v234
	v_add_u32_e32 v4, 2, v3
	s_nop 0
	v_cndmask_b32_e32 v99, v233, v99, vcc
	v_cmp_lt_i32_e32 vcc, v4, v234
	v_add_u32_e32 v4, 34, v3
	s_nop 0
	v_cndmask_b32_e32 v84, v233, v84, vcc
	v_cmp_lt_i32_e32 vcc, v4, v234
	v_add_u32_e32 v4, 3, v3
	s_nop 0
	v_cndmask_b32_e32 v100, v233, v100, vcc
	v_cmp_lt_i32_e32 vcc, v4, v234
	v_add_u32_e32 v4, 35, v3
	s_nop 0
	v_cndmask_b32_e32 v85, v233, v85, vcc
	v_cmp_lt_i32_e32 vcc, v4, v234
	v_add_u32_e32 v4, 8, v3
	s_nop 0
	v_cndmask_b32_e32 v101, v233, v101, vcc
	v_cmp_lt_i32_e32 vcc, v4, v234
	v_add_u32_e32 v4, 40, v3
	s_nop 0
	v_cndmask_b32_e32 v86, v233, v86, vcc
	v_cmp_lt_i32_e32 vcc, v4, v234
	v_add_u32_e32 v4, 9, v3
	s_nop 0
	v_cndmask_b32_e32 v102, v233, v102, vcc
	v_cmp_lt_i32_e32 vcc, v4, v234
	v_add_u32_e32 v4, 41, v3
	s_nop 0
	v_cndmask_b32_e32 v87, v233, v87, vcc
	v_cmp_lt_i32_e32 vcc, v4, v234
	v_add_u32_e32 v4, 10, v3
	s_nop 0
	v_cndmask_b32_e32 v103, v233, v103, vcc
	v_cmp_lt_i32_e32 vcc, v4, v234
	v_add_u32_e32 v4, 42, v3
	s_nop 0
	v_cndmask_b32_e32 v88, v233, v88, vcc
	v_cmp_lt_i32_e32 vcc, v4, v234
	v_add_u32_e32 v4, 11, v3
	s_nop 0
	v_cndmask_b32_e32 v104, v233, v104, vcc
	v_cmp_lt_i32_e32 vcc, v4, v234
	v_add_u32_e32 v4, 43, v3
	s_nop 0
	v_cndmask_b32_e32 v89, v233, v89, vcc
	v_cmp_lt_i32_e32 vcc, v4, v234
	v_add_u32_e32 v4, 16, v3
	s_nop 0
	v_cndmask_b32_e32 v105, v233, v105, vcc
	v_cmp_lt_i32_e32 vcc, v4, v234
	v_add_u32_e32 v4, 48, v3
	s_nop 0
	v_cndmask_b32_e32 v90, v233, v90, vcc
	v_cmp_lt_i32_e32 vcc, v4, v234
	v_add_u32_e32 v4, 17, v3
	s_nop 0
	v_cndmask_b32_e32 v106, v233, v106, vcc
	v_cmp_lt_i32_e32 vcc, v4, v234
	v_add_u32_e32 v4, 49, v3
	s_nop 0
	v_cndmask_b32_e32 v91, v233, v91, vcc
	v_cmp_lt_i32_e32 vcc, v4, v234
	v_add_u32_e32 v4, 18, v3
	s_nop 0
	v_cndmask_b32_e32 v107, v233, v107, vcc
	v_cmp_lt_i32_e32 vcc, v4, v234
	v_add_u32_e32 v4, 50, v3
	s_nop 0
	v_cndmask_b32_e32 v92, v233, v92, vcc
	v_cmp_lt_i32_e32 vcc, v4, v234
	v_add_u32_e32 v4, 19, v3
	s_nop 0
	v_cndmask_b32_e32 v108, v233, v108, vcc
	v_cmp_lt_i32_e32 vcc, v4, v234
	v_add_u32_e32 v4, 51, v3
	s_nop 0
	v_cndmask_b32_e32 v93, v233, v93, vcc
	v_cmp_lt_i32_e32 vcc, v4, v234
	v_add_u32_e32 v4, 24, v3
	s_nop 0
	v_cndmask_b32_e32 v109, v233, v109, vcc
	v_cmp_lt_i32_e32 vcc, v4, v234
	v_add_u32_e32 v4, 56, v3
	s_nop 0
	v_cndmask_b32_e32 v94, v233, v94, vcc
	v_cmp_lt_i32_e32 vcc, v4, v234
	v_add_u32_e32 v4, 25, v3
	s_nop 0
	v_cndmask_b32_e32 v110, v233, v110, vcc
	v_cmp_lt_i32_e32 vcc, v4, v234
	v_add_u32_e32 v4, 57, v3
	s_nop 0
	v_cndmask_b32_e32 v95, v233, v95, vcc
	v_cmp_lt_i32_e32 vcc, v4, v234
	v_add_u32_e32 v4, 26, v3
	s_nop 0
	v_cndmask_b32_e32 v111, v233, v111, vcc
	v_cmp_lt_i32_e32 vcc, v4, v234
	v_add_u32_e32 v4, 58, v3
	s_nop 0
	v_cndmask_b32_e32 v96, v233, v96, vcc
	v_cmp_lt_i32_e32 vcc, v4, v234
	v_add_u32_e32 v4, 27, v3
	v_add_u32_e32 v3, 59, v3
	v_cndmask_b32_e32 v112, v233, v112, vcc
	v_cmp_lt_i32_e32 vcc, v4, v234
	s_nop 1
	v_cndmask_b32_e32 v97, v233, v97, vcc
	v_cmp_lt_i32_e32 vcc, v3, v234
	s_nop 1
	v_cndmask_b32_e32 v113, v233, v113, vcc

.LBB0_2288:
	s_waitcnt lgkmcnt(0)
	s_cmp_ge_u32 s33, s24
	s_barrier
	s_cbranch_scc1 .LBB0_2290
	s_add_i32 s52, s6, -1
	s_ashr_i32 s53, s52, 31
	s_lshl_b64 s[52:53], s[52:53], 6
	v_mov_b32_e32 v237, s53
	v_or_b32_e32 v236, s52, v193
	v_lshlrev_b64 v[236:237], 11, v[236:237]
	v_mov_b32_e32 v241, s53
	v_or_b32_e32 v240, s52, v194
	v_lshl_add_u64 v[238:239], v[186:187], 0, v[236:237]
	v_lshlrev_b64 v[240:241], 11, v[240:241]
	v_lshl_add_u64 v[236:237], v[188:189], 0, v[236:237]
	v_lshl_add_u64 v[242:243], v[186:187], 0, v[240:241]
	global_load_dwordx4 v[154:157], v[238:239], off
	global_load_dwordx4 v[162:165], v[242:243], off
	v_lshl_add_u64 v[238:239], v[188:189], 0, v[240:241]
	global_load_dwordx4 v[170:173], v[236:237], off
	global_load_dwordx4 v[174:177], v[238:239], off
.LBB0_2290:
	s_add_i32 s6, s6, -2
	s_andn2_b64 vcc, exec, s[26:27]
	s_addk_i32 s31, 0xff80
	s_cbranch_vccnz .LBB0_2276
	s_cmp_eq_u32 s59, 2
	s_cbranch_scc0 .Lst1_epi_chk1
	s_mov_b32 s59, 0
	s_mov_b32 s60, 2
	s_branch .Lst1_tail1

.Lst1_epi:
	s_nop 15
	s_nop 7
	s_lshl_b64 s[20:21], s[20:21], 11
	v_readlane_b32 s6, v255, 4
	s_add_u32 s6, s6, s20
	v_readlane_b32 s20, v255, 2
	s_addc_u32 s21, s20, s21
	s_lshl_b32 s20, s25, 1
	s_add_u32 s20, s6, s20
	s_addc_u32 s21, s21, 0
	v_lshlrev_b32_e32 v4, 1, v216
	v_mov_b32_e32 v5, v2
	v_lshl_add_u64 v[4:5], s[20:21], 0, v[4:5]
	v_lshl_add_u64 v[4:5], v[4:5], 0, v[180:181]
	v_cvt_pk_bf16_f32 v3, v66, s0
	global_store_short v[4:5], v3, off
	v_cvt_pk_bf16_f32 v3, v50, s0
	global_store_short v[4:5], v3, off offset:64
	v_cvt_pk_bf16_f32 v3, v34, s0
	global_store_short v[4:5], v3, off offset:128
	v_cvt_pk_bf16_f32 v3, v18, s0
	global_store_short v[4:5], v3, off offset:192
	v_cvt_pk_bf16_f32 v3, v67, s0
	global_store_short v[4:5], v3, off offset:2048
	v_cvt_pk_bf16_f32 v3, v51, s0
	global_store_short v[4:5], v3, off offset:2112
	v_cvt_pk_bf16_f32 v3, v35, s0
	global_store_short v[4:5], v3, off offset:2176
	v_cvt_pk_bf16_f32 v3, v19, s0
	v_add_co_u32_e32 v6, vcc, s16, v4
	global_store_short v[4:5], v3, off offset:2240
	v_cvt_pk_bf16_f32 v3, v68, s0
	v_addc_co_u32_e32 v7, vcc, 0, v5, vcc
	global_store_short v[6:7], v3, off
	v_cvt_pk_bf16_f32 v3, v52, s0
	global_store_short v[6:7], v3, off offset:64
	v_cvt_pk_bf16_f32 v3, v36, s0
	global_store_short v[6:7], v3, off offset:128
	v_cvt_pk_bf16_f32 v3, v20, s0
	global_store_short v[6:7], v3, off offset:192
	v_cvt_pk_bf16_f32 v3, v69, s0
	global_store_short v[6:7], v3, off offset:2048
	v_cvt_pk_bf16_f32 v3, v53, s0
	global_store_short v[6:7], v3, off offset:2112
	v_cvt_pk_bf16_f32 v3, v37, s0
	global_store_short v[6:7], v3, off offset:2176
	v_cvt_pk_bf16_f32 v3, v21, s0
	global_store_short v[6:7], v3, off offset:2240
	v_add_co_u32_e32 v6, vcc, s17, v4
	v_cvt_pk_bf16_f32 v3, v70, s0
	s_nop 0
	v_addc_co_u32_e32 v7, vcc, 0, v5, vcc
	v_add_co_u32_e32 v8, vcc, s18, v4
	s_add_i32 s23, s23, s9
	s_nop 0
	v_addc_co_u32_e32 v9, vcc, 0, v5, vcc
	global_store_short v[8:9], v3, off offset:-4096
	v_cvt_pk_bf16_f32 v3, v54, s0
	global_store_short v[6:7], v3, off offset:64
	v_cvt_pk_bf16_f32 v3, v38, s0
	global_store_short v[6:7], v3, off offset:128
	v_cvt_pk_bf16_f32 v3, v22, s0
	global_store_short v[6:7], v3, off offset:192
	v_cvt_pk_bf16_f32 v3, v71, s0
	global_store_short v[6:7], v3, off offset:2048
	v_cvt_pk_bf16_f32 v3, v55, s0
	global_store_short v[6:7], v3, off offset:2112
	v_cvt_pk_bf16_f32 v3, v39, s0
	global_store_short v[6:7], v3, off offset:2176
	v_cvt_pk_bf16_f32 v3, v23, s0
	global_store_short v[6:7], v3, off offset:2240
	v_cvt_pk_bf16_f32 v3, v72, s0
	global_store_short v[8:9], v3, off
	v_cvt_pk_bf16_f32 v3, v56, s0
	global_store_short v[8:9], v3, off offset:64
	v_cvt_pk_bf16_f32 v3, v40, s0
	global_store_short v[8:9], v3, off offset:128
	v_cvt_pk_bf16_f32 v3, v24, s0
	global_store_short v[8:9], v3, off offset:192
	v_cvt_pk_bf16_f32 v3, v73, s0
	global_store_short v[8:9], v3, off offset:2048
	v_cvt_pk_bf16_f32 v3, v57, s0
	global_store_short v[8:9], v3, off offset:2112
	v_cvt_pk_bf16_f32 v3, v41, s0
	v_add_co_u32_e32 v6, vcc, s10, v4
	global_store_short v[8:9], v3, off offset:2176
	v_cvt_pk_bf16_f32 v3, v25, s0
	v_addc_co_u32_e32 v7, vcc, 0, v5, vcc
	global_store_short v[8:9], v3, off offset:2240
	v_add_co_u32_e32 v8, vcc, s19, v4
	v_cvt_pk_bf16_f32 v3, v74, s0
	s_nop 0
	v_addc_co_u32_e32 v9, vcc, 0, v5, vcc
	global_store_short v[8:9], v3, off offset:-4096
	v_cvt_pk_bf16_f32 v3, v58, s0
	global_store_short v[6:7], v3, off offset:64
	v_cvt_pk_bf16_f32 v3, v42, s0
	global_store_short v[6:7], v3, off offset:128
	v_cvt_pk_bf16_f32 v3, v26, s0
	global_store_short v[6:7], v3, off offset:192
	v_cvt_pk_bf16_f32 v3, v75, s0
	global_store_short v[6:7], v3, off offset:2048
	v_cvt_pk_bf16_f32 v3, v59, s0
	global_store_short v[6:7], v3, off offset:2112
	v_cvt_pk_bf16_f32 v3, v43, s0
	global_store_short v[6:7], v3, off offset:2176
	v_cvt_pk_bf16_f32 v3, v27, s0
	global_store_short v[6:7], v3, off offset:2240
	v_cvt_pk_bf16_f32 v3, v76, s0
	global_store_short v[8:9], v3, off
	v_cvt_pk_bf16_f32 v3, v60, s0
	global_store_short v[8:9], v3, off offset:64
	v_cvt_pk_bf16_f32 v3, v44, s0
	global_store_short v[8:9], v3, off offset:128
	v_cvt_pk_bf16_f32 v3, v28, s0
	global_store_short v[8:9], v3, off offset:192
	v_cvt_pk_bf16_f32 v3, v77, s0
	global_store_short v[8:9], v3, off offset:2048
	v_cvt_pk_bf16_f32 v3, v61, s0
	v_add_co_u32_e32 v6, vcc, s11, v4
	global_store_short v[8:9], v3, off offset:2112
	v_cvt_pk_bf16_f32 v3, v45, s0
	v_addc_co_u32_e32 v7, vcc, 0, v5, vcc
	global_store_short v[8:9], v3, off offset:2176
	v_cvt_pk_bf16_f32 v3, v29, s0
	v_add_co_u32_e32 v4, vcc, s22, v4
	global_store_short v[8:9], v3, off offset:2240
	v_cvt_pk_bf16_f32 v3, v78, s0
	v_addc_co_u32_e32 v5, vcc, 0, v5, vcc
	global_store_short v[4:5], v3, off offset:-4096
	v_cvt_pk_bf16_f32 v3, v62, s0
	global_store_short v[6:7], v3, off offset:64
	v_cvt_pk_bf16_f32 v3, v46, s0
	global_store_short v[6:7], v3, off offset:128
	v_cvt_pk_bf16_f32 v3, v30, s0
	global_store_short v[6:7], v3, off offset:192
	v_cvt_pk_bf16_f32 v3, v79, s0
	global_store_short v[6:7], v3, off offset:2048
	v_cvt_pk_bf16_f32 v3, v63, s0
	global_store_short v[6:7], v3, off offset:2112
	v_cvt_pk_bf16_f32 v3, v47, s0
	global_store_short v[6:7], v3, off offset:2176
	v_cvt_pk_bf16_f32 v3, v31, s0
	global_store_short v[6:7], v3, off offset:2240
	v_cvt_pk_bf16_f32 v3, v80, s0
	global_store_short v[4:5], v3, off
	v_cvt_pk_bf16_f32 v3, v64, s0
	global_store_short v[4:5], v3, off offset:64
	v_cvt_pk_bf16_f32 v3, v48, s0
	global_store_short v[4:5], v3, off offset:128
	v_cvt_pk_bf16_f32 v3, v32, s0
	global_store_short v[4:5], v3, off offset:192
	v_cvt_pk_bf16_f32 v3, v81, s0
	global_store_short v[4:5], v3, off offset:2048
	v_cvt_pk_bf16_f32 v3, v65, s0
	global_store_short v[4:5], v3, off offset:2112
	v_cvt_pk_bf16_f32 v3, v49, s0
	global_store_short v[4:5], v3, off offset:2176
	v_cvt_pk_bf16_f32 v3, v33, s0
	s_cmpk_gt_i32 s23, 0xff
	global_store_short v[4:5], v3, off offset:2240
	s_cbranch_scc0 .LBB0_2275
